# speedup vs baseline: 1.0092x; 1.0089x over previous
.LBB1_1:
	s_and_b32 s0, s29, 0x10000
	v_add_u32_e32 v211, s0, v209
	v_add_u32_e32 v242, s0, v210
	ds_read_b128 v[212:215], v242 offset:0
	ds_read_b128 v[216:219], v242 offset:2048
	ds_read_b128 v[220:223], v242 offset:4096
	ds_read_b128 v[224:227], v242 offset:6144
	ds_read_b128 v[228:231], v211 offset:0
	ds_read_b128 v[232:235], v211 offset:2048
	ds_read_b128 v[236:239], v211 offset:4096
	ds_read_b128 v[244:247], v211 offset:6144
	ds_read_b128 v[248:251], v211 offset:8192
	ds_read_b128 v[252:255], v211 offset:10240
	s_waitcnt lgkmcnt(5)
	v_mfma_f32_16x16x32_bf16 v[174:177], v[212:215], v[228:231], v[174:177]
	v_mfma_f32_16x16x32_bf16 v[170:173], v[216:219], v[228:231], v[170:173]
	v_mfma_f32_16x16x32_bf16 v[166:169], v[220:223], v[228:231], v[166:169]
	v_mfma_f32_16x16x32_bf16 v[162:165], v[224:227], v[228:231], v[162:165]
	ds_read_b128 v[228:231], v211 offset:12288
	s_waitcnt lgkmcnt(5)
	v_mfma_f32_16x16x32_bf16 v[158:161], v[212:215], v[232:235], v[158:161]
	v_mfma_f32_16x16x32_bf16 v[154:157], v[216:219], v[232:235], v[154:157]
	v_mfma_f32_16x16x32_bf16 v[150:153], v[220:223], v[232:235], v[150:153]
	v_mfma_f32_16x16x32_bf16 v[146:149], v[224:227], v[232:235], v[146:149]
	ds_read_b128 v[232:235], v211 offset:14336
	s_waitcnt lgkmcnt(5)
	v_mfma_f32_16x16x32_bf16 v[142:145], v[212:215], v[236:239], v[142:145]
	v_mfma_f32_16x16x32_bf16 v[138:141], v[216:219], v[236:239], v[138:141]
	v_mfma_f32_16x16x32_bf16 v[134:137], v[220:223], v[236:239], v[134:137]
	v_mfma_f32_16x16x32_bf16 v[130:133], v[224:227], v[236:239], v[130:133]
	s_waitcnt lgkmcnt(4)
	v_mfma_f32_16x16x32_bf16 v[126:129], v[212:215], v[244:247], v[126:129]
	v_mfma_f32_16x16x32_bf16 v[122:125], v[216:219], v[244:247], v[122:125]
	v_mfma_f32_16x16x32_bf16 v[118:121], v[220:223], v[244:247], v[118:121]
	v_mfma_f32_16x16x32_bf16 v[114:117], v[224:227], v[244:247], v[114:117]
	s_waitcnt lgkmcnt(3)
	v_mfma_f32_16x16x32_bf16 v[110:113], v[212:215], v[248:251], v[110:113]
	v_mfma_f32_16x16x32_bf16 v[106:109], v[216:219], v[248:251], v[106:109]
	v_mfma_f32_16x16x32_bf16 v[102:105], v[220:223], v[248:251], v[102:105]
	v_mfma_f32_16x16x32_bf16 v[98:101], v[224:227], v[248:251], v[98:101]
	s_waitcnt lgkmcnt(2)
	v_mfma_f32_16x16x32_bf16 v[94:97], v[212:215], v[252:255], v[94:97]
	v_mfma_f32_16x16x32_bf16 v[90:93], v[216:219], v[252:255], v[90:93]
	v_mfma_f32_16x16x32_bf16 v[86:89], v[220:223], v[252:255], v[86:89]
	v_mfma_f32_16x16x32_bf16 v[82:85], v[224:227], v[252:255], v[82:85]
	s_waitcnt lgkmcnt(1)
	v_mfma_f32_16x16x32_bf16 v[78:81], v[212:215], v[228:231], v[78:81]
	v_mfma_f32_16x16x32_bf16 v[74:77], v[216:219], v[228:231], v[74:77]
	v_mfma_f32_16x16x32_bf16 v[70:73], v[220:223], v[228:231], v[70:73]
	v_mfma_f32_16x16x32_bf16 v[66:69], v[224:227], v[228:231], v[66:69]
	s_waitcnt lgkmcnt(0)
	v_mfma_f32_16x16x32_bf16 v[62:65], v[212:215], v[232:235], v[62:65]
	v_mfma_f32_16x16x32_bf16 v[58:61], v[216:219], v[232:235], v[58:61]
	v_mfma_f32_16x16x32_bf16 v[54:57], v[220:223], v[232:235], v[54:57]
	v_mfma_f32_16x16x32_bf16 v[50:53], v[224:227], v[232:235], v[50:53]
	s_xor_b32 s0, s0, 0x10000
	s_and_b32 s1, s22, 0x3c0
	s_add_i32 s23, s0, 0
	s_lshl_b32 s0, s1, 2
	s_add_u32 s20, s25, s0
	s_waitcnt vmcnt(10)
	v_cvt_pk_bf16_f32 v46, v46, v47
	v_cvt_pk_bf16_f32 v47, v48, v49
	v_cvt_pk_bf16_f32 v48, v42, v43
	v_cvt_pk_bf16_f32 v49, v44, v45
	s_waitcnt vmcnt(8)
	v_cvt_pk_bf16_f32 v38, v38, v39
	v_cvt_pk_bf16_f32 v39, v40, v41
	v_cvt_pk_bf16_f32 v40, v34, v35
	v_add_u32_e32 v34, s23, v208
	s_addc_u32 s21, s26, 0
	s_lshl_b32 s0, s1, 1
	v_cvt_pk_bf16_f32 v41, v36, v37
	v_lshlrev_b32_e32 v182, 2, v178
	v_add_u32_e32 v35, s23, v205
	v_add_u32_e32 v36, s23, v206
	v_add_u32_e32 v37, s23, v207
	ds_write_b128 v34, v[46:49]
	ds_write_b128 v35, v[38:41]
	s_waitcnt vmcnt(7)
	ds_write_b128 v36, v[30:33] offset:32768
	s_waitcnt vmcnt(6)
	ds_write_b128 v37, v[26:29] offset:32768
	v_lshl_add_u64 v[26:27], s[20:21], 0, v[180:181]
	v_lshl_add_u64 v[28:29], s[20:21], 0, v[184:185]
	s_add_u32 s0, s27, s0
	v_lshl_add_u64 v[26:27], v[26:27], 0, v[182:183]
	v_lshl_add_u64 v[28:29], v[28:29], 0, v[182:183]
	s_addc_u32 s1, s28, 0
	v_lshlrev_b32_e32 v240, 1, v178
	v_mov_b32_e32 v241, v183
	global_load_dwordx4 v[42:45], v[26:27], off offset:16
	global_load_dwordx4 v[46:49], v[26:27], off
	global_load_dwordx4 v[34:37], v[28:29], off offset:16
	global_load_dwordx4 v[38:41], v[28:29], off
	v_lshl_add_u64 v[26:27], s[0:1], 0, v[186:187]
	v_lshl_add_u64 v[28:29], s[0:1], 0, v[188:189]
	v_lshl_add_u64 v[26:27], v[26:27], 0, v[240:241]
	v_lshl_add_u64 v[28:29], v[28:29], 0, v[240:241]
	global_load_dwordx4 v[30:33], v[26:27], off
	s_nop 0
	global_load_dwordx4 v[26:29], v[28:29], off
	ds_read_b128 v[212:215], v242 offset:1024
	ds_read_b128 v[216:219], v242 offset:3072
	ds_read_b128 v[220:223], v242 offset:5120
	ds_read_b128 v[224:227], v242 offset:7168
	ds_read_b128 v[228:231], v211 offset:1024
	ds_read_b128 v[232:235], v211 offset:3072
	ds_read_b128 v[236:239], v211 offset:5120
	ds_read_b128 v[244:247], v211 offset:7168
	ds_read_b128 v[248:251], v211 offset:9216
	ds_read_b128 v[252:255], v211 offset:11264
	s_waitcnt lgkmcnt(5)
	v_mfma_f32_16x16x32_bf16 v[174:177], v[212:215], v[228:231], v[174:177]
	v_mfma_f32_16x16x32_bf16 v[170:173], v[216:219], v[228:231], v[170:173]
	v_mfma_f32_16x16x32_bf16 v[166:169], v[220:223], v[228:231], v[166:169]
	v_mfma_f32_16x16x32_bf16 v[162:165], v[224:227], v[228:231], v[162:165]
	ds_read_b128 v[228:231], v211 offset:13312
	s_waitcnt lgkmcnt(5)
	v_mfma_f32_16x16x32_bf16 v[158:161], v[212:215], v[232:235], v[158:161]
	v_mfma_f32_16x16x32_bf16 v[154:157], v[216:219], v[232:235], v[154:157]
	v_mfma_f32_16x16x32_bf16 v[150:153], v[220:223], v[232:235], v[150:153]
	v_mfma_f32_16x16x32_bf16 v[146:149], v[224:227], v[232:235], v[146:149]
	ds_read_b128 v[232:235], v211 offset:15360
	s_waitcnt lgkmcnt(5)
	v_mfma_f32_16x16x32_bf16 v[142:145], v[212:215], v[236:239], v[142:145]
	v_mfma_f32_16x16x32_bf16 v[138:141], v[216:219], v[236:239], v[138:141]
	v_mfma_f32_16x16x32_bf16 v[134:137], v[220:223], v[236:239], v[134:137]
	v_mfma_f32_16x16x32_bf16 v[130:133], v[224:227], v[236:239], v[130:133]
	s_waitcnt lgkmcnt(4)
	v_mfma_f32_16x16x32_bf16 v[126:129], v[212:215], v[244:247], v[126:129]
	v_mfma_f32_16x16x32_bf16 v[122:125], v[216:219], v[244:247], v[122:125]
	v_mfma_f32_16x16x32_bf16 v[118:121], v[220:223], v[244:247], v[118:121]
	v_mfma_f32_16x16x32_bf16 v[114:117], v[224:227], v[244:247], v[114:117]
	s_waitcnt lgkmcnt(3)
	v_mfma_f32_16x16x32_bf16 v[110:113], v[212:215], v[248:251], v[110:113]
	v_mfma_f32_16x16x32_bf16 v[106:109], v[216:219], v[248:251], v[106:109]
	v_mfma_f32_16x16x32_bf16 v[102:105], v[220:223], v[248:251], v[102:105]
	v_mfma_f32_16x16x32_bf16 v[98:101], v[224:227], v[248:251], v[98:101]
	s_waitcnt lgkmcnt(2)
	v_mfma_f32_16x16x32_bf16 v[94:97], v[212:215], v[252:255], v[94:97]
	v_mfma_f32_16x16x32_bf16 v[90:93], v[216:219], v[252:255], v[90:93]
	v_mfma_f32_16x16x32_bf16 v[86:89], v[220:223], v[252:255], v[86:89]
	v_mfma_f32_16x16x32_bf16 v[82:85], v[224:227], v[252:255], v[82:85]
	s_waitcnt lgkmcnt(1)
	v_mfma_f32_16x16x32_bf16 v[78:81], v[212:215], v[228:231], v[78:81]
	v_mfma_f32_16x16x32_bf16 v[74:77], v[216:219], v[228:231], v[74:77]
	v_mfma_f32_16x16x32_bf16 v[70:73], v[220:223], v[228:231], v[70:73]
	v_mfma_f32_16x16x32_bf16 v[66:69], v[224:227], v[228:231], v[66:69]
	s_waitcnt lgkmcnt(0)
	v_mfma_f32_16x16x32_bf16 v[62:65], v[212:215], v[232:235], v[62:65]
	v_mfma_f32_16x16x32_bf16 v[58:61], v[216:219], v[232:235], v[58:61]
	v_mfma_f32_16x16x32_bf16 v[54:57], v[220:223], v[232:235], v[54:57]
	v_mfma_f32_16x16x32_bf16 v[50:53], v[224:227], v[232:235], v[50:53]
	s_waitcnt vmcnt(10)
	v_cvt_pk_bf16_f32 v22, v22, v23
	v_cvt_pk_bf16_f32 v23, v24, v25
	v_cvt_pk_bf16_f32 v24, v6, v7
	v_cvt_pk_bf16_f32 v25, v8, v9
	v_add_u32_e32 v6, s23, v204
	s_waitcnt vmcnt(9)
	v_cvt_pk_bf16_f32 v8, v2, v3
	v_add_u32_e32 v2, s23, v201
	ds_write_b128 v6, v[22:25]
	s_waitcnt vmcnt(8)
	v_cvt_pk_bf16_f32 v6, v10, v11
	v_cvt_pk_bf16_f32 v7, v12, v13
	v_cvt_pk_bf16_f32 v9, v4, v5
	ds_write_b128 v2, v[6:9]
	v_add_u32_e32 v2, s23, v202
	s_waitcnt vmcnt(7)
	ds_write_b128 v2, v[18:21] offset:32768
	v_add_u32_e32 v2, s23, v203
	s_waitcnt vmcnt(6)
	ds_write_b128 v2, v[14:17] offset:32768
	v_lshl_add_u64 v[2:3], s[20:21], 0, v[190:191]
	v_lshl_add_u64 v[2:3], v[2:3], 0, v[182:183]
	global_load_dwordx4 v[6:9], v[2:3], off offset:16
	global_load_dwordx4 v[22:25], v[2:3], off
	v_lshl_add_u64 v[2:3], s[20:21], 0, v[192:193]
	v_lshl_add_u64 v[14:15], s[0:1], 0, v[194:195]
	v_lshl_add_u64 v[16:17], s[0:1], 0, v[196:197]
	v_lshl_add_u64 v[10:11], v[2:3], 0, v[182:183]
	v_lshl_add_u64 v[14:15], v[14:15], 0, v[240:241]
	v_lshl_add_u64 v[16:17], v[16:17], 0, v[240:241]
	global_load_dwordx4 v[2:5], v[10:11], off offset:16
	s_nop 0
	global_load_dwordx4 v[10:13], v[10:11], off
	s_nop 0
	global_load_dwordx4 v[18:21], v[14:15], off
	s_nop 0
	global_load_dwordx4 v[14:17], v[16:17], off
	s_waitcnt lgkmcnt(0)
	s_add_i32 s22, s22, 64
	s_add_i32 s29, s29, 0x10000
	s_cmp_lg_u32 s29, 0xe0000
	s_barrier
	s_cbranch_scc1 .LBB1_1
	s_lshl_b64 s[0:1], s[18:19], 24
	ds_read_b128 v[180:183], v210 offset:0
	ds_read_b128 v[184:187], v210 offset:0x800
	ds_read_b128 v[188:191], v210 offset:0x1000
	ds_read_b128 v[192:195], v210 offset:0x1800
	ds_read_b128 v[212:215], v209 offset:0
	ds_read_b128 v[216:219], v209 offset:0x800
	ds_read_b128 v[220:223], v209 offset:0x1000
	s_waitcnt lgkmcnt(0)
	s_add_u32 s0, s10, s0
	s_addc_u32 s18, s11, s1
	s_lshl_b32 s19, s24, 1
	s_mov_b32 s1, 0
	s_add_u32 s0, s0, s19
	s_waitcnt lgkmcnt(2)
	s_addc_u32 s20, s18, 0
	v_mfma_f32_16x16x32_bf16 v[174:177], v[180:183], v[212:215], v[174:177]
	v_mfma_f32_16x16x32_bf16 v[170:173], v[184:187], v[212:215], v[170:173]
	v_mfma_f32_16x16x32_bf16 v[166:169], v[188:191], v[212:215], v[166:169]
	v_mfma_f32_16x16x32_bf16 v[162:165], v[192:195], v[212:215], v[162:165]
	ds_read_b128 v[212:215], v209 offset:0x1800
	s_waitcnt lgkmcnt(2)
	v_mfma_f32_16x16x32_bf16 v[158:161], v[180:183], v[216:219], v[158:161]
	v_mfma_f32_16x16x32_bf16 v[154:157], v[184:187], v[216:219], v[154:157]
	v_mfma_f32_16x16x32_bf16 v[150:153], v[188:191], v[216:219], v[150:153]
	v_mfma_f32_16x16x32_bf16 v[146:149], v[192:195], v[216:219], v[146:149]
	ds_read_b128 v[216:219], v209 offset:0x2000
	s_waitcnt lgkmcnt(2)
	v_mfma_f32_16x16x32_bf16 v[142:145], v[180:183], v[220:223], v[142:145]
	v_mfma_f32_16x16x32_bf16 v[138:141], v[184:187], v[220:223], v[138:141]
	v_mfma_f32_16x16x32_bf16 v[134:137], v[188:191], v[220:223], v[134:137]
	v_mfma_f32_16x16x32_bf16 v[130:133], v[192:195], v[220:223], v[130:133]
	ds_read_b128 v[220:223], v209 offset:0x2800
	s_waitcnt lgkmcnt(2)
	v_mfma_f32_16x16x32_bf16 v[126:129], v[180:183], v[212:215], v[126:129]
	v_mfma_f32_16x16x32_bf16 v[122:125], v[184:187], v[212:215], v[122:125]
	v_mfma_f32_16x16x32_bf16 v[118:121], v[188:191], v[212:215], v[118:121]
	v_mfma_f32_16x16x32_bf16 v[114:117], v[192:195], v[212:215], v[114:117]
	ds_read_b128 v[212:215], v209 offset:0x3000
	s_waitcnt lgkmcnt(2)
	v_mfma_f32_16x16x32_bf16 v[110:113], v[180:183], v[216:219], v[110:113]
	v_mfma_f32_16x16x32_bf16 v[106:109], v[184:187], v[216:219], v[106:109]
	v_mfma_f32_16x16x32_bf16 v[102:105], v[188:191], v[216:219], v[102:105]
	v_mfma_f32_16x16x32_bf16 v[98:101], v[192:195], v[216:219], v[98:101]
	ds_read_b128 v[216:219], v209 offset:0x3800
	s_waitcnt lgkmcnt(2)
	v_mfma_f32_16x16x32_bf16 v[94:97], v[180:183], v[220:223], v[94:97]
	v_mfma_f32_16x16x32_bf16 v[90:93], v[184:187], v[220:223], v[90:93]
	v_mfma_f32_16x16x32_bf16 v[86:89], v[188:191], v[220:223], v[86:89]
	v_mfma_f32_16x16x32_bf16 v[82:85], v[192:195], v[220:223], v[82:85]
	s_waitcnt lgkmcnt(1)
	v_mfma_f32_16x16x32_bf16 v[78:81], v[180:183], v[212:215], v[78:81]
	v_mfma_f32_16x16x32_bf16 v[74:77], v[184:187], v[212:215], v[74:77]
	v_mfma_f32_16x16x32_bf16 v[70:73], v[188:191], v[212:215], v[70:73]
	v_mfma_f32_16x16x32_bf16 v[66:69], v[192:195], v[212:215], v[66:69]
	s_waitcnt lgkmcnt(0)
	v_mfma_f32_16x16x32_bf16 v[62:65], v[180:183], v[216:219], v[62:65]
	v_mfma_f32_16x16x32_bf16 v[58:61], v[184:187], v[216:219], v[58:61]
	v_mfma_f32_16x16x32_bf16 v[54:57], v[188:191], v[216:219], v[54:57]
	v_mfma_f32_16x16x32_bf16 v[50:53], v[192:195], v[216:219], v[50:53]
	s_add_i32 s18, 0, 0x10000
	s_waitcnt vmcnt(10)
	v_cvt_pk_bf16_f32 v46, v46, v47
	v_cvt_pk_bf16_f32 v47, v48, v49
	v_cvt_pk_bf16_f32 v48, v42, v43
	v_add_u32_e32 v42, s18, v208
	s_waitcnt vmcnt(8)
	v_cvt_pk_bf16_f32 v38, v38, v39
	v_cvt_pk_bf16_f32 v39, v40, v41
	v_cvt_pk_bf16_f32 v40, v34, v35
	v_add_u32_e32 v34, s18, v205
	s_add_i32 s19, 0, 0x18000
	v_cvt_pk_bf16_f32 v49, v44, v45
	ds_write_b128 v42, v[46:49]
	v_cvt_pk_bf16_f32 v41, v36, v37
	ds_write_b128 v34, v[38:41]
	v_add_u32_e32 v34, s19, v206
	s_waitcnt vmcnt(7)
	ds_write_b128 v34, v[30:33]
	v_add_u32_e32 v30, s19, v207
	s_waitcnt vmcnt(6)
	ds_write_b128 v30, v[26:29]
	ds_read_b128 v[26:29], v210 offset:0x400
	ds_read_b128 v[30:33], v210 offset:0xc00
	ds_read_b128 v[34:37], v210 offset:0x1400
	ds_read_b128 v[38:41], v210 offset:0x1c00
	ds_read_b128 v[42:45], v209 offset:0x400
	ds_read_b128 v[46:49], v209 offset:0xc00
	ds_read_b128 v[180:183], v209 offset:0x1400
	s_waitcnt lgkmcnt(2)
	v_mfma_f32_16x16x32_bf16 v[174:177], v[26:29], v[42:45], v[174:177]
	v_mfma_f32_16x16x32_bf16 v[170:173], v[30:33], v[42:45], v[170:173]
	v_mfma_f32_16x16x32_bf16 v[166:169], v[34:37], v[42:45], v[166:169]
	v_mfma_f32_16x16x32_bf16 v[42:45], v[38:41], v[42:45], v[162:165]
	ds_read_b128 v[162:165], v209 offset:0x1c00
	s_waitcnt lgkmcnt(2)
	v_mfma_f32_16x16x32_bf16 v[158:161], v[26:29], v[46:49], v[158:161]
	v_mfma_f32_16x16x32_bf16 v[154:157], v[30:33], v[46:49], v[154:157]
	v_mfma_f32_16x16x32_bf16 v[150:153], v[34:37], v[46:49], v[150:153]
	v_mfma_f32_16x16x32_bf16 v[46:49], v[38:41], v[46:49], v[146:149]
	ds_read_b128 v[146:149], v209 offset:0x2400
	s_waitcnt lgkmcnt(2)
	v_mfma_f32_16x16x32_bf16 v[142:145], v[26:29], v[180:183], v[142:145]
	v_mfma_f32_16x16x32_bf16 v[138:141], v[30:33], v[180:183], v[138:141]
	v_mfma_f32_16x16x32_bf16 v[134:137], v[34:37], v[180:183], v[134:137]
	v_mfma_f32_16x16x32_bf16 v[130:133], v[38:41], v[180:183], v[130:133]
	ds_read_b128 v[180:183], v209 offset:0x2c00
	s_waitcnt lgkmcnt(2)
	v_mfma_f32_16x16x32_bf16 v[126:129], v[26:29], v[162:165], v[126:129]
	v_mfma_f32_16x16x32_bf16 v[122:125], v[30:33], v[162:165], v[122:125]
	v_mfma_f32_16x16x32_bf16 v[118:121], v[34:37], v[162:165], v[118:121]
	v_mfma_f32_16x16x32_bf16 v[114:117], v[38:41], v[162:165], v[114:117]
	ds_read_b128 v[162:165], v209 offset:0x3400
	s_waitcnt lgkmcnt(2)
	v_mfma_f32_16x16x32_bf16 v[110:113], v[26:29], v[146:149], v[110:113]
	v_mfma_f32_16x16x32_bf16 v[106:109], v[30:33], v[146:149], v[106:109]
	v_mfma_f32_16x16x32_bf16 v[102:105], v[34:37], v[146:149], v[102:105]
	v_mfma_f32_16x16x32_bf16 v[98:101], v[38:41], v[146:149], v[98:101]
	ds_read_b128 v[146:149], v209 offset:0x3c00
	s_waitcnt lgkmcnt(2)
	v_mfma_f32_16x16x32_bf16 v[94:97], v[26:29], v[180:183], v[94:97]
	v_mfma_f32_16x16x32_bf16 v[90:93], v[30:33], v[180:183], v[90:93]
	v_mfma_f32_16x16x32_bf16 v[86:89], v[34:37], v[180:183], v[86:89]
	v_mfma_f32_16x16x32_bf16 v[82:85], v[38:41], v[180:183], v[82:85]
	s_waitcnt lgkmcnt(1)
	v_mfma_f32_16x16x32_bf16 v[78:81], v[26:29], v[162:165], v[78:81]
	v_mfma_f32_16x16x32_bf16 v[74:77], v[30:33], v[162:165], v[74:77]
	v_mfma_f32_16x16x32_bf16 v[70:73], v[34:37], v[162:165], v[70:73]
	v_mfma_f32_16x16x32_bf16 v[66:69], v[38:41], v[162:165], v[66:69]
	s_waitcnt lgkmcnt(0)
	v_mfma_f32_16x16x32_bf16 v[26:29], v[26:29], v[146:149], v[62:65]
	v_mfma_f32_16x16x32_bf16 v[30:33], v[30:33], v[146:149], v[58:61]
	v_mfma_f32_16x16x32_bf16 v[34:37], v[34:37], v[146:149], v[54:57]
	v_mfma_f32_16x16x32_bf16 v[38:41], v[38:41], v[146:149], v[50:53]
	s_waitcnt vmcnt(4)
	v_cvt_pk_bf16_f32 v22, v22, v23
	v_cvt_pk_bf16_f32 v23, v24, v25
	v_cvt_pk_bf16_f32 v24, v6, v7
	v_cvt_pk_bf16_f32 v25, v8, v9
	v_add_u32_e32 v6, s18, v204
	s_waitcnt vmcnt(3)
	v_cvt_pk_bf16_f32 v8, v2, v3
	v_add_u32_e32 v2, s18, v201
	ds_write_b128 v6, v[22:25]
	s_waitcnt vmcnt(2)
	v_cvt_pk_bf16_f32 v6, v10, v11
	v_cvt_pk_bf16_f32 v7, v12, v13
	v_cvt_pk_bf16_f32 v9, v4, v5
	ds_write_b128 v2, v[6:9]
	v_add_u32_e32 v2, s19, v202
	s_waitcnt vmcnt(1)
	ds_write_b128 v2, v[18:21]
	v_add_u32_e32 v2, s19, v203
	s_waitcnt vmcnt(0)
	ds_write_b128 v2, v[14:17]
	s_waitcnt lgkmcnt(0)
	s_barrier
	v_add_u32_e32 v178, 0x10000, v209
	v_add_u32_e32 v196, 0x10000, v210
	ds_read_b128 v[2:5], v196 offset:0
	ds_read_b128 v[6:9], v196 offset:0x800
	ds_read_b128 v[10:13], v196 offset:0x1000
	ds_read_b128 v[14:17], v196 offset:0x1800
	ds_read_b128 v[18:21], v178 offset:0
	s_and_b64 s[16:17], s[16:17], exec
	ds_read_b128 v[22:25], v178 offset:0x800
	ds_read_b128 v[50:53], v178 offset:0x1000
	s_waitcnt lgkmcnt(2)
	s_cselect_b32 s5, s5, s7
	s_cselect_b32 s4, s4, s6
	s_lshl_b32 s6, s3, 10
	v_mfma_f32_16x16x32_bf16 v[54:57], v[2:5], v[18:21], v[174:177]
	s_add_u32 s6, s4, s6
	s_addc_u32 s7, s5, 0
	s_lshl_b32 s3, s3, 9
	v_mfma_f32_16x16x32_bf16 v[58:61], v[6:9], v[18:21], v[170:173]
	s_add_u32 s4, s0, s3
	s_addc_u32 s5, s20, 0
	v_mfma_f32_16x16x32_bf16 v[62:65], v[10:13], v[18:21], v[166:169]
	v_mfma_f32_16x16x32_bf16 v[18:21], v[14:17], v[18:21], v[42:45]
	ds_read_b128 v[42:45], v178 offset:0x1800
	s_waitcnt lgkmcnt(2)
	v_mfma_f32_16x16x32_bf16 v[146:149], v[2:5], v[22:25], v[158:161]
	v_mfma_f32_16x16x32_bf16 v[154:157], v[6:9], v[22:25], v[154:157]
	v_mfma_f32_16x16x32_bf16 v[150:153], v[10:13], v[22:25], v[150:153]
	v_mfma_f32_16x16x32_bf16 v[22:25], v[14:17], v[22:25], v[46:49]
	ds_read_b128 v[46:49], v178 offset:0x2000
	s_waitcnt lgkmcnt(2)
	v_mfma_f32_16x16x32_bf16 v[142:145], v[2:5], v[50:53], v[142:145]
	v_mfma_f32_16x16x32_bf16 v[138:141], v[6:9], v[50:53], v[138:141]
	v_mfma_f32_16x16x32_bf16 v[134:137], v[10:13], v[50:53], v[134:137]
	v_mfma_f32_16x16x32_bf16 v[50:53], v[14:17], v[50:53], v[130:133]
	ds_read_b128 v[130:133], v178 offset:0x2800
	s_waitcnt lgkmcnt(2)
	v_mfma_f32_16x16x32_bf16 v[126:129], v[2:5], v[42:45], v[126:129]
	v_mfma_f32_16x16x32_bf16 v[122:125], v[6:9], v[42:45], v[122:125]
	v_mfma_f32_16x16x32_bf16 v[118:121], v[10:13], v[42:45], v[118:121]
	v_mfma_f32_16x16x32_bf16 v[42:45], v[14:17], v[42:45], v[114:117]
	ds_read_b128 v[114:117], v178 offset:0x3000
	s_waitcnt lgkmcnt(2)
	v_mfma_f32_16x16x32_bf16 v[110:113], v[2:5], v[46:49], v[110:113]
	v_mfma_f32_16x16x32_bf16 v[106:109], v[6:9], v[46:49], v[106:109]
	v_mfma_f32_16x16x32_bf16 v[102:105], v[10:13], v[46:49], v[102:105]
	v_mfma_f32_16x16x32_bf16 v[98:101], v[14:17], v[46:49], v[98:101]
	ds_read_b128 v[46:49], v178 offset:0x3800
	s_waitcnt lgkmcnt(2)
	v_mfma_f32_16x16x32_bf16 v[158:161], v[2:5], v[130:133], v[94:97]
	v_mfma_f32_16x16x32_bf16 v[162:165], v[6:9], v[130:133], v[90:93]
	v_mfma_f32_16x16x32_bf16 v[166:169], v[10:13], v[130:133], v[86:89]
	v_mfma_f32_16x16x32_bf16 v[130:133], v[14:17], v[130:133], v[82:85]
	s_waitcnt lgkmcnt(1)
	v_mfma_f32_16x16x32_bf16 v[66:69], v[14:17], v[114:117], v[66:69]
	v_mfma_f32_16x16x32_bf16 v[170:173], v[2:5], v[114:117], v[78:81]
	v_mfma_f32_16x16x32_bf16 v[174:177], v[6:9], v[114:117], v[74:77]
	v_mfma_f32_16x16x32_bf16 v[180:183], v[10:13], v[114:117], v[70:73]
	s_waitcnt lgkmcnt(0)
	v_mfma_f32_16x16x32_bf16 v[2:5], v[2:5], v[46:49], v[26:29]
	v_mfma_f32_16x16x32_bf16 v[114:117], v[6:9], v[46:49], v[30:33]
	v_mfma_f32_16x16x32_bf16 v[34:37], v[10:13], v[46:49], v[34:37]
	v_mfma_f32_16x16x32_bf16 v[184:187], v[14:17], v[46:49], v[38:41]
	ds_read_b128 v[188:191], v196 offset:0x400
	ds_read_b128 v[192:195], v196 offset:0xc00
	ds_read_b128 v[202:205], v196 offset:0x1400
	ds_read_b128 v[206:209], v196 offset:0x1c00
	ds_read_b128 v[6:9], v178 offset:0x400
	ds_read_b128 v[10:13], v178 offset:0xc00
	ds_read_b128 v[14:17], v178 offset:0x1400
	s_waitcnt lgkmcnt(2)
	v_mfma_f32_16x16x32_bf16 v[94:97], v[192:195], v[6:9], v[58:61]
	v_mfma_f32_16x16x32_bf16 v[62:65], v[202:205], v[6:9], v[62:65]
	v_mfma_f32_16x16x32_bf16 v[30:33], v[206:209], v[6:9], v[18:21]
	v_mfma_f32_16x16x32_bf16 v[210:213], v[188:191], v[6:9], v[54:57]
	ds_read_b128 v[6:9], v178 offset:0x1c00
	s_waitcnt lgkmcnt(2)
	v_mfma_f32_16x16x32_bf16 v[90:93], v[192:195], v[10:13], v[154:157]
	v_mfma_f32_16x16x32_bf16 v[58:61], v[202:205], v[10:13], v[150:153]
	v_mfma_f32_16x16x32_bf16 v[26:29], v[206:209], v[10:13], v[22:25]
	v_mfma_f32_16x16x32_bf16 v[146:149], v[188:191], v[10:13], v[146:149]
	ds_read_b128 v[10:13], v178 offset:0x2400
	s_waitcnt lgkmcnt(2)
	v_mfma_f32_16x16x32_bf16 v[86:89], v[192:195], v[14:17], v[138:141]
	v_mfma_f32_16x16x32_bf16 v[54:57], v[202:205], v[14:17], v[134:137]
	v_mfma_f32_16x16x32_bf16 v[22:25], v[206:209], v[14:17], v[50:53]
	v_mfma_f32_16x16x32_bf16 v[142:145], v[188:191], v[14:17], v[142:145]
	ds_read_b128 v[38:41], v178 offset:0x2c00
	s_waitcnt lgkmcnt(2)
	v_mfma_f32_16x16x32_bf16 v[126:129], v[188:191], v[6:9], v[126:129]
	v_mfma_f32_16x16x32_bf16 v[82:85], v[192:195], v[6:9], v[122:125]
	v_mfma_f32_16x16x32_bf16 v[50:53], v[202:205], v[6:9], v[118:121]
	v_mfma_f32_16x16x32_bf16 v[18:21], v[206:209], v[6:9], v[42:45]
	ds_read_b128 v[6:9], v178 offset:0x3400
	s_waitcnt lgkmcnt(2)
	v_mfma_f32_16x16x32_bf16 v[110:113], v[188:191], v[10:13], v[110:113]
	v_mfma_f32_16x16x32_bf16 v[78:81], v[192:195], v[10:13], v[106:109]
	v_mfma_f32_16x16x32_bf16 v[46:49], v[202:205], v[10:13], v[102:105]
	v_mfma_f32_16x16x32_bf16 v[14:17], v[206:209], v[10:13], v[98:101]
	ds_read_b128 v[98:101], v178 offset:0x3c00
	s_waitcnt lgkmcnt(2)
	v_mfma_f32_16x16x32_bf16 v[106:109], v[188:191], v[38:41], v[158:161]
	v_mfma_f32_16x16x32_bf16 v[74:77], v[192:195], v[38:41], v[162:165]
	v_mfma_f32_16x16x32_bf16 v[42:45], v[202:205], v[38:41], v[166:169]
	v_mfma_f32_16x16x32_bf16 v[10:13], v[206:209], v[38:41], v[130:133]
	s_waitcnt lgkmcnt(1)
	v_mfma_f32_16x16x32_bf16 v[118:121], v[188:191], v[6:9], v[170:173]
	v_mfma_f32_16x16x32_bf16 v[70:73], v[192:195], v[6:9], v[174:177]
	v_mfma_f32_16x16x32_bf16 v[38:41], v[202:205], v[6:9], v[180:183]
	v_mfma_f32_16x16x32_bf16 v[6:9], v[206:209], v[6:9], v[66:69]
	s_waitcnt lgkmcnt(0)
	v_mfma_f32_16x16x32_bf16 v[122:125], v[188:191], v[98:101], v[2:5]
	v_mfma_f32_16x16x32_bf16 v[66:69], v[192:195], v[98:101], v[114:117]
	v_mfma_f32_16x16x32_bf16 v[34:37], v[202:205], v[98:101], v[34:37]
	v_mfma_f32_16x16x32_bf16 v[2:5], v[206:209], v[98:101], v[184:187]
	v_lshrrev_b32_e32 v98, 2, v199
	v_and_b32_e32 v98, 12, v98
	v_lshl_or_b32 v104, v200, 6, v98
	v_lshlrev_b32_e32 v105, 2, v104
	s_waitcnt lgkmcnt(0)
	s_barrier
	global_load_dwordx4 v[114:117], v105, s[6:7]
	v_lshrrev_b32_e32 v98, 1, v199
	v_lshlrev_b32_e32 v99, 16, v198
	v_lshlrev_b32_e32 v100, 9, v179
	v_and_b32_e32 v102, 8, v98
	v_lshrrev_b32_e32 v98, 3, v104
	v_add3_u32 v103, 0, v99, v100
	v_xor_b32_e32 v130, v98, v179
	v_bitop3_b32 v131, v98, v179, 16 bitop3:0x1e
	global_load_dwordx4 v[98:101], v105, s[6:7] offset:64
	v_lshlrev_b32_e32 v130, 4, v130
	v_lshlrev_b32_e32 v131, 4, v131
	v_add3_u32 v130, v103, v130, v102
	v_add3_u32 v131, v103, v131, v102
	s_movk_i32 s0, 0x200
	s_waitcnt vmcnt(1)
	v_add_f32_e32 v132, v210, v114
	v_add_f32_e32 v133, v211, v115
	v_add_f32_e32 v134, v212, v116
	v_add_f32_e32 v135, v213, v117
	v_add_f32_e32 v140, v142, v114
	v_add_f32_e32 v141, v143, v115
	v_add_f32_e32 v142, v144, v116
	v_add_f32_e32 v143, v145, v117
	v_add_f32_e32 v110, v110, v114
	v_add_f32_e32 v111, v111, v115
	v_add_f32_e32 v106, v106, v114
	v_add_f32_e32 v107, v107, v115
	v_add_f32_e32 v136, v146, v114
	v_add_f32_e32 v137, v147, v115
	v_add_f32_e32 v138, v148, v116
	v_add_f32_e32 v139, v149, v117
	v_add_f32_e32 v126, v126, v114
	v_add_f32_e32 v127, v127, v115
	v_add_f32_e32 v128, v128, v116
	v_add_f32_e32 v129, v129, v117
	v_add_f32_e32 v112, v112, v116
	v_add_f32_e32 v113, v113, v117
	v_add_f32_e32 v108, v108, v116
	v_add_f32_e32 v109, v109, v117
	v_max_f32_e32 v132, 0, v132
	v_max_f32_e32 v133, 0, v133
	v_max_f32_e32 v134, 0, v134
	v_max_f32_e32 v135, 0, v135
	v_max_f32_e32 v140, 0, v140
	v_max_f32_e32 v141, 0, v141
	v_max_f32_e32 v142, 0, v142
	v_max_f32_e32 v143, 0, v143
	v_max_f32_e32 v144, 0, v110
	v_max_f32_e32 v145, 0, v111
	v_max_f32_e32 v148, 0, v106
	v_max_f32_e32 v149, 0, v107
	v_cvt_pk_bf16_f32 v106, v132, v133
	v_cvt_pk_bf16_f32 v107, v134, v135
	v_cvt_pk_bf16_f32 v110, v140, v141
	v_cvt_pk_bf16_f32 v111, v142, v143
	v_add_f32_e32 v118, v118, v114
	v_add_f32_e32 v119, v119, v115
	v_max_f32_e32 v136, 0, v136
	v_max_f32_e32 v137, 0, v137
	v_max_f32_e32 v138, 0, v138
	v_max_f32_e32 v139, 0, v139
	v_max_f32_e32 v126, 0, v126
	v_max_f32_e32 v127, 0, v127
	v_max_f32_e32 v128, 0, v128
	v_max_f32_e32 v129, 0, v129
	v_max_f32_e32 v146, 0, v112
	v_max_f32_e32 v147, 0, v113
	v_max_f32_e32 v150, 0, v108
	v_max_f32_e32 v151, 0, v109
	v_cvt_pk_bf16_f32 v108, v136, v137
	v_cvt_pk_bf16_f32 v109, v138, v139
	v_cvt_pk_bf16_f32 v112, v126, v127
	v_cvt_pk_bf16_f32 v113, v128, v129
	ds_write2st64_b64 v130, v[106:107], v[110:111] offset1:32
	ds_write2st64_b64 v131, v[108:109], v[112:113] offset0:16 offset1:48
	v_add_f32_e32 v106, v121, v117
	v_add_f32_e32 v120, v120, v116
	v_max_f32_e32 v152, 0, v118
	v_max_f32_e32 v153, 0, v119
	v_max_f32_e32 v107, 0, v106
	v_cvt_pk_bf16_f32 v106, v152, v153
	v_max_f32_e32 v120, 0, v120
	v_cvt_pk_bf16_f32 v118, v144, v145
	v_cvt_pk_bf16_f32 v119, v146, v147
	v_cvt_pk_bf16_f32 v107, v120, v107
	ds_write2st64_b64 v130, v[118:119], v[106:107] offset0:64 offset1:96
	v_add_f32_e32 v106, v122, v114
	v_max_f32_e32 v106, 0, v106
	v_add_f32_e32 v107, v123, v115
	v_max_f32_e32 v107, 0, v107
	v_add_f32_e32 v108, v124, v116
	v_add_f32_e32 v109, v125, v117
	v_cvt_pk_bf16_f32 v106, v106, v107
	v_cvt_pk_bf16_f32 v126, v148, v149
	v_cvt_pk_bf16_f32 v127, v150, v151
	v_max_f32_e32 v108, 0, v108
	v_max_f32_e32 v109, 0, v109
	v_cvt_pk_bf16_f32 v107, v108, v109
	ds_write2st64_b64 v131, v[126:127], v[106:107] offset0:80 offset1:112
	v_or_b32_e32 v106, 16, v104
	s_waitcnt vmcnt(0)
	v_add_f32_e32 v94, v94, v98
	v_add_f32_e32 v95, v95, v99
	v_add_f32_e32 v96, v96, v100
	v_lshrrev_b32_e32 v106, 3, v106
	v_max_f32_e32 v94, 0, v94
	v_max_f32_e32 v95, 0, v95
	v_max_f32_e32 v96, 0, v96
	v_add_f32_e32 v97, v97, v101
	v_max_f32_e32 v97, 0, v97
	v_cvt_pk_bf16_f32 v94, v94, v95
	v_cvt_pk_bf16_f32 v95, v96, v97
	v_xor_b32_e32 v96, v106, v179
	v_lshlrev_b32_e32 v96, 4, v96
	v_add3_u32 v107, v103, v96, v102
	v_add_f32_e32 v90, v90, v98
	v_add_f32_e32 v91, v91, v99
	v_add_f32_e32 v92, v92, v100
	ds_write_b64 v107, v[94:95]
	v_max_f32_e32 v90, 0, v90
	v_max_f32_e32 v91, 0, v91
	global_load_dwordx4 v[94:97], v105, s[6:7] offset:128
	v_max_f32_e32 v92, 0, v92
	v_add_f32_e32 v93, v93, v101
	v_max_f32_e32 v93, 0, v93
	v_cvt_pk_bf16_f32 v90, v90, v91
	v_cvt_pk_bf16_f32 v91, v92, v93
	v_bitop3_b32 v92, v106, v179, 16 bitop3:0x1e
	v_add_f32_e32 v66, v66, v98
	v_lshlrev_b32_e32 v92, 4, v92
	v_add_f32_e32 v86, v86, v98
	v_add_f32_e32 v87, v87, v99
	v_add_f32_e32 v82, v82, v98
	v_add_f32_e32 v83, v83, v99
	v_add_f32_e32 v78, v78, v98
	v_add_f32_e32 v79, v79, v99
	v_add_f32_e32 v74, v74, v98
	v_add_f32_e32 v75, v75, v99
	v_add_f32_e32 v70, v70, v98
	v_add_f32_e32 v71, v71, v99
	v_max_f32_e32 v66, 0, v66
	v_add_f32_e32 v67, v67, v99
	v_add3_u32 v92, v103, v92, v102
	v_max_f32_e32 v86, 0, v86
	v_max_f32_e32 v87, 0, v87
	v_add_f32_e32 v88, v88, v100
	v_add_f32_e32 v89, v89, v101
	v_max_f32_e32 v82, 0, v82
	v_max_f32_e32 v83, 0, v83
	v_add_f32_e32 v84, v84, v100
	v_add_f32_e32 v85, v85, v101
	v_max_f32_e32 v78, 0, v78
	v_max_f32_e32 v79, 0, v79
	v_add_f32_e32 v80, v80, v100
	v_add_f32_e32 v81, v81, v101
	v_max_f32_e32 v74, 0, v74
	v_max_f32_e32 v75, 0, v75
	v_add_f32_e32 v76, v76, v100
	v_add_f32_e32 v77, v77, v101
	v_max_f32_e32 v70, 0, v70
	v_max_f32_e32 v71, 0, v71
	v_add_f32_e32 v72, v72, v100
	v_add_f32_e32 v73, v73, v101
	v_max_f32_e32 v67, 0, v67
	v_add_f32_e32 v68, v68, v100
	v_add_f32_e32 v69, v69, v101
	v_cvt_pk_bf16_f32 v66, v66, v67
	ds_write_b64 v92, v[90:91] offset:8192
	v_max_f32_e32 v88, 0, v88
	v_max_f32_e32 v89, 0, v89
	v_cvt_pk_bf16_f32 v86, v86, v87
	v_cvt_pk_bf16_f32 v87, v88, v89
	ds_write_b64 v107, v[86:87] offset:16384
	v_max_f32_e32 v84, 0, v84
	v_max_f32_e32 v85, 0, v85
	v_cvt_pk_bf16_f32 v82, v82, v83
	v_cvt_pk_bf16_f32 v83, v84, v85
	ds_write_b64 v92, v[82:83] offset:24576
	v_max_f32_e32 v80, 0, v80
	v_max_f32_e32 v81, 0, v81
	v_cvt_pk_bf16_f32 v78, v78, v79
	v_cvt_pk_bf16_f32 v79, v80, v81
	ds_write_b64 v107, v[78:79] offset:32768
	v_max_f32_e32 v76, 0, v76
	v_max_f32_e32 v77, 0, v77
	v_cvt_pk_bf16_f32 v74, v74, v75
	v_cvt_pk_bf16_f32 v75, v76, v77
	ds_write_b64 v92, v[74:75] offset:40960
	v_max_f32_e32 v72, 0, v72
	v_max_f32_e32 v73, 0, v73
	v_cvt_pk_bf16_f32 v70, v70, v71
	v_cvt_pk_bf16_f32 v71, v72, v73
	ds_write_b64 v107, v[70:71] offset:49152
	v_max_f32_e32 v68, 0, v68
	v_max_f32_e32 v69, 0, v69
	v_cvt_pk_bf16_f32 v67, v68, v69
	ds_write_b64 v92, v[66:67] offset:57344
	v_or_b32_e32 v66, 32, v104
	v_lshrrev_b32_e32 v70, 3, v66
	global_load_dwordx4 v[66:69], v105, s[6:7] offset:192
	s_waitcnt vmcnt(1)
	v_add_f32_e32 v62, v62, v94
	v_add_f32_e32 v63, v63, v95
	v_add_f32_e32 v64, v64, v96
	v_add_f32_e32 v58, v58, v94
	v_add_f32_e32 v59, v59, v95
	v_add_f32_e32 v60, v60, v96
	v_max_f32_e32 v62, 0, v62
	v_max_f32_e32 v63, 0, v63
	v_max_f32_e32 v64, 0, v64
	v_add_f32_e32 v65, v65, v97
	v_max_f32_e32 v58, 0, v58
	v_max_f32_e32 v59, 0, v59
	v_max_f32_e32 v60, 0, v60
	v_add_f32_e32 v61, v61, v97
	v_max_f32_e32 v65, 0, v65
	v_cvt_pk_bf16_f32 v62, v62, v63
	v_cvt_pk_bf16_f32 v63, v64, v65
	v_xor_b32_e32 v64, v70, v179
	v_max_f32_e32 v61, 0, v61
	v_cvt_pk_bf16_f32 v58, v58, v59
	v_cvt_pk_bf16_f32 v59, v60, v61
	v_bitop3_b32 v60, v70, v179, 16 bitop3:0x1e
	v_add_f32_e32 v34, v34, v94
	v_lshlrev_b32_e32 v64, 4, v64
	v_lshlrev_b32_e32 v60, 4, v60
	v_add_f32_e32 v54, v54, v94
	v_add_f32_e32 v55, v55, v95
	v_add_f32_e32 v50, v50, v94
	v_add_f32_e32 v51, v51, v95
	v_add_f32_e32 v46, v46, v94
	v_add_f32_e32 v47, v47, v95
	v_add_f32_e32 v42, v42, v94
	v_add_f32_e32 v43, v43, v95
	v_add_f32_e32 v38, v38, v94
	v_add_f32_e32 v39, v39, v95
	v_max_f32_e32 v34, 0, v34
	v_add_f32_e32 v35, v35, v95
	v_add3_u32 v64, v103, v64, v102
	v_add3_u32 v60, v103, v60, v102
	v_max_f32_e32 v54, 0, v54
	v_max_f32_e32 v55, 0, v55
	v_add_f32_e32 v56, v56, v96
	v_add_f32_e32 v57, v57, v97
	v_max_f32_e32 v50, 0, v50
	v_max_f32_e32 v51, 0, v51
	v_add_f32_e32 v52, v52, v96
	v_add_f32_e32 v53, v53, v97
	v_max_f32_e32 v46, 0, v46
	v_max_f32_e32 v47, 0, v47
	v_add_f32_e32 v48, v48, v96
	v_add_f32_e32 v49, v49, v97
	v_max_f32_e32 v42, 0, v42
	v_max_f32_e32 v43, 0, v43
	v_add_f32_e32 v44, v44, v96
	v_add_f32_e32 v45, v45, v97
	v_max_f32_e32 v38, 0, v38
	v_max_f32_e32 v39, 0, v39
	v_add_f32_e32 v40, v40, v96
	v_add_f32_e32 v41, v41, v97
	v_max_f32_e32 v35, 0, v35
	v_add_f32_e32 v36, v36, v96
	v_add_f32_e32 v37, v37, v97
	v_cvt_pk_bf16_f32 v34, v34, v35
	ds_write_b64 v64, v[62:63]
	ds_write_b64 v60, v[58:59] offset:8192
	v_max_f32_e32 v56, 0, v56
	v_max_f32_e32 v57, 0, v57
	v_cvt_pk_bf16_f32 v54, v54, v55
	v_cvt_pk_bf16_f32 v55, v56, v57
	ds_write_b64 v64, v[54:55] offset:16384
	v_max_f32_e32 v52, 0, v52
	v_max_f32_e32 v53, 0, v53
	v_cvt_pk_bf16_f32 v50, v50, v51
	v_cvt_pk_bf16_f32 v51, v52, v53
	ds_write_b64 v60, v[50:51] offset:24576
	v_max_f32_e32 v48, 0, v48
	v_max_f32_e32 v49, 0, v49
	v_cvt_pk_bf16_f32 v46, v46, v47
	v_cvt_pk_bf16_f32 v47, v48, v49
	ds_write_b64 v64, v[46:47] offset:32768
	v_max_f32_e32 v44, 0, v44
	v_max_f32_e32 v45, 0, v45
	v_cvt_pk_bf16_f32 v42, v42, v43
	v_cvt_pk_bf16_f32 v43, v44, v45
	ds_write_b64 v60, v[42:43] offset:40960
	v_max_f32_e32 v40, 0, v40
	v_max_f32_e32 v41, 0, v41
	v_cvt_pk_bf16_f32 v38, v38, v39
	v_cvt_pk_bf16_f32 v39, v40, v41
	ds_write_b64 v64, v[38:39] offset:49152
	v_max_f32_e32 v36, 0, v36
	v_max_f32_e32 v37, 0, v37
	v_cvt_pk_bf16_f32 v35, v36, v37
	ds_write_b64 v60, v[34:35] offset:57344
	v_or_b32_e32 v34, 48, v104
	s_waitcnt vmcnt(0)
	v_add_f32_e32 v30, v30, v66
	v_add_f32_e32 v31, v31, v67
	v_add_f32_e32 v32, v32, v68
	v_add_f32_e32 v26, v26, v66
	v_add_f32_e32 v27, v27, v67
	v_add_f32_e32 v28, v28, v68
	v_lshrrev_b32_e32 v34, 3, v34
	v_max_f32_e32 v30, 0, v30
	v_max_f32_e32 v31, 0, v31
	v_max_f32_e32 v32, 0, v32
	v_add_f32_e32 v33, v33, v69
	v_max_f32_e32 v26, 0, v26
	v_max_f32_e32 v27, 0, v27
	v_max_f32_e32 v28, 0, v28
	v_add_f32_e32 v29, v29, v69
	v_max_f32_e32 v33, 0, v33
	v_cvt_pk_bf16_f32 v30, v30, v31
	v_cvt_pk_bf16_f32 v31, v32, v33
	v_xor_b32_e32 v32, v34, v179
	v_max_f32_e32 v29, 0, v29
	v_cvt_pk_bf16_f32 v26, v26, v27
	v_cvt_pk_bf16_f32 v27, v28, v29
	v_bitop3_b32 v28, v34, v179, 16 bitop3:0x1e
	v_add_f32_e32 v2, v2, v66
	v_lshlrev_b32_e32 v32, 4, v32
	v_lshlrev_b32_e32 v28, 4, v28
	v_add_f32_e32 v22, v22, v66
	v_add_f32_e32 v23, v23, v67
	v_add_f32_e32 v18, v18, v66
	v_add_f32_e32 v19, v19, v67
	v_add_f32_e32 v14, v14, v66
	v_add_f32_e32 v15, v15, v67
	v_add_f32_e32 v10, v10, v66
	v_add_f32_e32 v11, v11, v67
	v_add_f32_e32 v6, v6, v66
	v_add_f32_e32 v7, v7, v67
	v_max_f32_e32 v2, 0, v2
	v_add_f32_e32 v3, v3, v67
	v_add3_u32 v32, v103, v32, v102
	v_add3_u32 v28, v103, v28, v102
	v_max_f32_e32 v22, 0, v22
	v_max_f32_e32 v23, 0, v23
	v_add_f32_e32 v24, v24, v68
	v_add_f32_e32 v25, v25, v69
	v_max_f32_e32 v18, 0, v18
	v_max_f32_e32 v19, 0, v19
	v_add_f32_e32 v20, v20, v68
	v_add_f32_e32 v21, v21, v69
	v_max_f32_e32 v14, 0, v14
	v_max_f32_e32 v15, 0, v15
	v_add_f32_e32 v16, v16, v68
	v_add_f32_e32 v17, v17, v69
	v_max_f32_e32 v10, 0, v10
	v_max_f32_e32 v11, 0, v11
	v_add_f32_e32 v12, v12, v68
	v_add_f32_e32 v13, v13, v69
	v_max_f32_e32 v6, 0, v6
	v_max_f32_e32 v7, 0, v7
	v_add_f32_e32 v8, v8, v68
	v_add_f32_e32 v9, v9, v69
	v_max_f32_e32 v3, 0, v3
	v_add_f32_e32 v4, v4, v68
	v_add_f32_e32 v5, v5, v69
	v_cvt_pk_bf16_f32 v2, v2, v3
	ds_write_b64 v32, v[30:31]
	ds_write_b64 v28, v[26:27] offset:8192
	v_max_f32_e32 v24, 0, v24
	v_max_f32_e32 v25, 0, v25
	v_cvt_pk_bf16_f32 v22, v22, v23
	v_cvt_pk_bf16_f32 v23, v24, v25
	ds_write_b64 v32, v[22:23] offset:16384
	v_max_f32_e32 v20, 0, v20
	v_max_f32_e32 v21, 0, v21
	v_cvt_pk_bf16_f32 v18, v18, v19
	v_cvt_pk_bf16_f32 v19, v20, v21
	ds_write_b64 v28, v[18:19] offset:24576
	v_max_f32_e32 v16, 0, v16
	v_max_f32_e32 v17, 0, v17
	v_cvt_pk_bf16_f32 v14, v14, v15
	v_cvt_pk_bf16_f32 v15, v16, v17
	ds_write_b64 v32, v[14:15] offset:32768
	v_max_f32_e32 v12, 0, v12
	v_max_f32_e32 v13, 0, v13
	v_cvt_pk_bf16_f32 v10, v10, v11
	v_cvt_pk_bf16_f32 v11, v12, v13
	ds_write_b64 v28, v[10:11] offset:40960
	v_max_f32_e32 v8, 0, v8
	v_max_f32_e32 v9, 0, v9
	v_cvt_pk_bf16_f32 v6, v6, v7
	v_cvt_pk_bf16_f32 v7, v8, v9
	ds_write_b64 v32, v[6:7] offset:49152
	v_max_f32_e32 v4, 0, v4
	v_max_f32_e32 v5, 0, v5
	v_cvt_pk_bf16_f32 v3, v4, v5
	ds_write_b64 v28, v[2:3] offset:57344
	v_and_b32_e32 v2, 0x1f0, v1
	v_lshrrev_b32_e32 v1, 5, v0
	v_xor_b32_e32 v4, v1, v0
	v_mov_b32_e32 v3, 0
	v_lshlrev_b32_e32 v4, 4, v4
	v_lshl_add_u64 v[12:13], s[4:5], 0, v[2:3]
	v_lshlrev_b32_e32 v2, 9, v1
	v_and_b32_e32 v16, 0x1f0, v4
	v_add3_u32 v2, 0, v2, v16
	s_waitcnt lgkmcnt(0)
	s_barrier
	ds_read_b128 v[4:7], v2
	v_lshlrev_b32_e32 v2, 11, v1
	v_lshl_add_u64 v[14:15], v[12:13], 0, v[2:3]
	v_or_b32_e32 v2, 0x200, v0
	v_lshrrev_b32_e32 v2, 5, v2
	v_xor_b32_e32 v9, v2, v0
	v_lshlrev_b32_e32 v9, 4, v9
	v_lshlrev_b32_e32 v8, 9, v2
	v_and_b32_e32 v9, 0x1f0, v9
	v_add3_u32 v8, 0, v8, v9
	ds_read_b128 v[8:11], v8
	v_lshlrev_b32_e32 v2, 11, v2
	s_waitcnt lgkmcnt(1)
	global_store_dwordx4 v[14:15], v[4:7], off sc1
	s_nop 1
	v_lshl_add_u64 v[4:5], v[12:13], 0, v[2:3]
	s_waitcnt lgkmcnt(0)
	global_store_dwordx4 v[4:5], v[8:11], off sc1
	v_or_b32_e32 v2, 32, v1
	v_lshlrev_b32_e32 v4, 9, v2
	v_or_b32_e32 v8, 0x600, v0
	v_lshrrev_b32_e32 v17, 5, v8
	v_xor_b32_e32 v9, v17, v0
	v_lshlrev_b32_e32 v9, 4, v9
	v_add3_u32 v4, 0, v4, v16
	v_lshlrev_b32_e32 v8, 9, v17
	v_and_b32_e32 v9, 0x1f0, v9
	ds_read_b128 v[4:7], v4
	v_add3_u32 v8, 0, v8, v9
	ds_read_b128 v[8:11], v8
	v_lshlrev_b32_e32 v2, 11, v2
	v_lshl_add_u64 v[14:15], v[12:13], 0, v[2:3]
	v_lshlrev_b32_e32 v2, 11, v17
	s_waitcnt lgkmcnt(1)
	global_store_dwordx4 v[14:15], v[4:7], off sc1
	s_nop 1
	v_lshl_add_u64 v[4:5], v[12:13], 0, v[2:3]
	s_waitcnt lgkmcnt(0)
	global_store_dwordx4 v[4:5], v[8:11], off sc1
	v_or_b32_e32 v2, 64, v1
	v_lshlrev_b32_e32 v4, 9, v2
	v_or_b32_e32 v8, 0xa00, v0
	v_lshrrev_b32_e32 v17, 5, v8
	v_xor_b32_e32 v9, v17, v0
	v_lshlrev_b32_e32 v9, 4, v9
	v_add3_u32 v4, 0, v4, v16
	v_lshlrev_b32_e32 v8, 9, v17
	v_and_b32_e32 v9, 0x1f0, v9
	ds_read_b128 v[4:7], v4
	v_add3_u32 v8, 0, v8, v9
	ds_read_b128 v[8:11], v8
	v_lshlrev_b32_e32 v2, 11, v2
	v_lshl_add_u64 v[14:15], v[12:13], 0, v[2:3]
	v_lshlrev_b32_e32 v2, 11, v17
	s_waitcnt lgkmcnt(1)
	global_store_dwordx4 v[14:15], v[4:7], off sc1
	s_nop 1
	v_lshl_add_u64 v[4:5], v[12:13], 0, v[2:3]
	s_waitcnt lgkmcnt(0)
	global_store_dwordx4 v[4:5], v[8:11], off sc1
	v_or_b32_e32 v2, 0x60, v1
	v_lshlrev_b32_e32 v4, 9, v2
	v_or_b32_e32 v8, 0xe00, v0
	v_lshrrev_b32_e32 v17, 5, v8
	v_xor_b32_e32 v9, v17, v0
	v_lshlrev_b32_e32 v9, 4, v9
	v_add3_u32 v4, 0, v4, v16
	v_lshlrev_b32_e32 v8, 9, v17
	v_and_b32_e32 v9, 0x1f0, v9
	ds_read_b128 v[4:7], v4
	v_add3_u32 v8, 0, v8, v9
	ds_read_b128 v[8:11], v8
	v_lshlrev_b32_e32 v2, 11, v2
	v_lshl_add_u64 v[14:15], v[12:13], 0, v[2:3]
	v_lshlrev_b32_e32 v2, 11, v17
	s_waitcnt lgkmcnt(1)
	global_store_dwordx4 v[14:15], v[4:7], off sc1
	s_nop 1
	v_lshl_add_u64 v[4:5], v[12:13], 0, v[2:3]
	s_waitcnt lgkmcnt(0)
	global_store_dwordx4 v[4:5], v[8:11], off sc1
	v_or_b32_e32 v2, 0x80, v1
	v_lshlrev_b32_e32 v4, 9, v2
	v_or_b32_e32 v8, 0x1200, v0
	v_lshrrev_b32_e32 v17, 5, v8
	v_xor_b32_e32 v9, v17, v0
	v_lshlrev_b32_e32 v9, 4, v9
	v_add3_u32 v4, 0, v4, v16
	v_lshlrev_b32_e32 v8, 9, v17
	v_and_b32_e32 v9, 0x1f0, v9
	ds_read_b128 v[4:7], v4
	v_add3_u32 v8, 0, v8, v9
	ds_read_b128 v[8:11], v8
	v_lshlrev_b32_e32 v2, 11, v2
	v_lshl_add_u64 v[14:15], v[12:13], 0, v[2:3]
	v_lshlrev_b32_e32 v2, 11, v17
	s_waitcnt lgkmcnt(1)
	global_store_dwordx4 v[14:15], v[4:7], off sc1
	s_nop 1
	v_lshl_add_u64 v[4:5], v[12:13], 0, v[2:3]
	s_waitcnt lgkmcnt(0)
	global_store_dwordx4 v[4:5], v[8:11], off sc1
	v_or_b32_e32 v2, 0xa0, v1
	v_lshlrev_b32_e32 v4, 9, v2
	v_or_b32_e32 v8, 0x1600, v0
	v_lshrrev_b32_e32 v17, 5, v8
	v_xor_b32_e32 v9, v17, v0
	v_lshlrev_b32_e32 v9, 4, v9
	v_add3_u32 v4, 0, v4, v16
	v_lshlrev_b32_e32 v8, 9, v17
	v_and_b32_e32 v9, 0x1f0, v9
	ds_read_b128 v[4:7], v4
	v_add3_u32 v8, 0, v8, v9
	ds_read_b128 v[8:11], v8
	v_lshlrev_b32_e32 v2, 11, v2
	v_lshl_add_u64 v[14:15], v[12:13], 0, v[2:3]
	v_lshlrev_b32_e32 v2, 11, v17
	s_waitcnt lgkmcnt(1)
	global_store_dwordx4 v[14:15], v[4:7], off sc1
	s_nop 1
	v_lshl_add_u64 v[4:5], v[12:13], 0, v[2:3]
	s_waitcnt lgkmcnt(0)
	global_store_dwordx4 v[4:5], v[8:11], off sc1
	v_or_b32_e32 v2, 0xc0, v1
	v_lshlrev_b32_e32 v4, 9, v2
	v_or_b32_e32 v8, 0x1a00, v0
	v_lshrrev_b32_e32 v17, 5, v8
	v_xor_b32_e32 v9, v17, v0
	v_add3_u32 v4, 0, v4, v16
	v_lshlrev_b32_e32 v9, 4, v9
	ds_read_b128 v[4:7], v4
	v_lshlrev_b32_e32 v8, 9, v17
	v_and_b32_e32 v9, 0x1f0, v9
	v_add3_u32 v8, 0, v8, v9
	ds_read_b128 v[8:11], v8
	v_lshlrev_b32_e32 v2, 11, v2
	v_lshl_add_u64 v[14:15], v[12:13], 0, v[2:3]
	v_lshlrev_b32_e32 v2, 11, v17
	v_or_b32_e32 v1, 0xe0, v1
	s_waitcnt lgkmcnt(1)
	global_store_dwordx4 v[14:15], v[4:7], off sc1
	s_nop 1
	v_lshl_add_u64 v[4:5], v[12:13], 0, v[2:3]
	v_lshlrev_b32_e32 v2, 9, v1
	v_add3_u32 v2, 0, v2, v16
	s_waitcnt lgkmcnt(0)
	global_store_dwordx4 v[4:5], v[8:11], off sc1
	ds_read_b128 v[4:7], v2
	v_lshlrev_b32_e32 v2, 11, v1
	v_or_b32_e32 v1, 0x1e00, v0
	v_lshrrev_b32_e32 v1, 5, v1
	v_xor_b32_e32 v9, v1, v0
	v_lshlrev_b32_e32 v9, 4, v9
	v_lshlrev_b32_e32 v8, 9, v1
	v_and_b32_e32 v9, 0x1f0, v9
	v_add3_u32 v8, 0, v8, v9
	ds_read_b128 v[8:11], v8
	v_lshl_add_u64 v[14:15], v[12:13], 0, v[2:3]
	v_lshlrev_b32_e32 v2, 11, v1
	s_waitcnt lgkmcnt(1)
	global_store_dwordx4 v[14:15], v[4:7], off sc1
	s_nop 1
	v_lshl_add_u64 v[4:5], v[12:13], 0, v[2:3]
	s_waitcnt lgkmcnt(0)
	global_store_dwordx4 v[4:5], v[8:11], off sc1
	s_waitcnt lgkmcnt(0)
	s_barrier
	s_lshl_b32 s3, s2, 3
	s_and_b32 s3, s3, 56
	s_ashr_i32 s17, s2, 5
	s_add_i32 s20, s3, s17
	s_ashr_i32 s21, s20, 31
	s_bfe_u32 s16, s2, 0x20003
	s_lshl_b64 s[4:5], s[20:21], 17
	s_lshl_b64 s[6:7], s[20:21], 19
	s_add_u32 s6, s12, s6
	s_addc_u32 s7, s13, s7
	s_lshl_b32 s3, s16, 19
	s_add_u32 s3, s14, s3
	v_ashrrev_i32_e32 v2, 6, v0
	v_lshlrev_b32_e32 v1, 4, v0
	s_addc_u32 s13, s15, 0
	v_lshlrev_b32_e32 v4, 9, v2
	v_and_b32_e32 v5, 0x1f0, v1
	s_add_u32 s12, s3, 0x400000
	v_and_or_b32 v32, v4, s0, v5
	v_lshlrev_b32_e32 v4, 5, v2
	v_and_b32_e32 v5, 48, v1
	s_addc_u32 s13, s13, 0
	v_bitop3_b32 v4, v4, v5, 32 bitop3:0x6c
	s_and_b32 s15, s2, 8
	s_add_i32 s3, s20, 3
	v_bfe_u32 v31, v0, 5, 1
	v_lshrrev_b32_e32 v34, 1, v4
	v_add_u32_e32 v4, s15, v2
	s_mov_b32 s20, 0x3ffffe
	v_and_or_b32 v30, v4, s20, v31
	v_bfe_i32 v5, v30, 0, 22
	v_bfe_u32 v4, v30, 21, 1
	v_add_u32_e32 v6, v5, v4
	v_lshlrev_b32_e32 v4, 3, v6
	v_and_b32_e32 v6, 0x7fffffe, v6
	s_lshl_b32 s0, s17, 4
	v_sub_u32_e32 v5, v5, v6
	s_and_b32 s17, s0, 16
	v_lshl_or_b32 v6, v5, 5, v34
	v_add_u32_e32 v5, s17, v2
	v_and_or_b32 v35, v5, s20, v31
	v_bfe_i32 v7, v35, 0, 22
	v_bfe_u32 v8, v35, 21, 1
	v_add_u32_e32 v8, v7, v8
	v_lshlrev_b32_e32 v9, 3, v8
	v_and_b32_e32 v8, 0x7fffffe, v8
	v_add_u32_e32 v5, 8, v5
	v_sub_u32_e32 v7, v7, v8
	v_and_or_b32 v36, v5, s20, v31
	v_lshl_or_b32 v98, v7, 5, v34
	v_bfe_i32 v5, v36, 0, 22
	v_bfe_u32 v7, v36, 21, 1
	v_add_u32_e32 v7, v5, v7
	v_lshrrev_b32_e32 v33, 6, v32
	v_lshlrev_b32_e32 v8, 3, v7
	v_and_b32_e32 v7, 0x7fffffe, v7
	s_and_b32 s3, s3, 15
	v_and_or_b32 v4, v4, -16, v33
	v_sub_u32_e32 v5, v5, v7
	v_and_or_b32 v14, v9, -16, v33
	v_lshl_or_b32 v100, v5, 5, v34
	v_ashrrev_i32_e32 v5, 31, v4
	s_lshl_b32 s14, s3, 6
	s_lshl_b32 s0, s3, 8
	s_lshl_b32 s2, s3, 7
	v_and_or_b32 v16, v8, -16, v33
	v_lshlrev_b64 v[4:5], 12, v[4:5]
	s_add_u32 s2, s12, s2
	v_ashrrev_i32_e32 v15, 31, v14
	v_lshl_add_u64 v[4:5], s[6:7], 0, v[4:5]
	v_ashrrev_i32_e32 v7, 31, v6
	s_addc_u32 s3, s13, 0
	v_lshlrev_b64 v[102:103], 11, v[14:15]
	v_ashrrev_i32_e32 v99, 31, v98
	v_ashrrev_i32_e32 v17, 31, v16
	v_lshl_add_u64 v[8:9], v[4:5], 0, s[0:1]
	v_lshlrev_b64 v[38:39], 2, v[6:7]
	v_lshl_add_u64 v[14:15], s[2:3], 0, v[102:103]
	v_lshlrev_b64 v[22:23], 1, v[98:99]
	v_lshlrev_b64 v[104:105], 11, v[16:17]
	v_ashrrev_i32_e32 v101, 31, v100
	v_lshl_add_u64 v[18:19], v[8:9], 0, v[38:39]
	v_lshl_add_u64 v[24:25], v[14:15], 0, v[22:23]
	v_lshl_add_u64 v[14:15], s[2:3], 0, v[104:105]
	v_lshlrev_b64 v[26:27], 1, v[100:101]
	global_load_dwordx4 v[6:9], v[18:19], off offset:16
	global_load_dwordx4 v[10:13], v[18:19], off
	v_lshl_add_u64 v[28:29], v[14:15], 0, v[26:27]
	global_load_dwordx4 v[14:17], v[24:25], off
	global_load_dwordx4 v[18:21], v[28:29], off
	v_lshlrev_b32_e32 v24, 10, v30
	v_or_b32_e32 v125, v24, v32
	v_xad_u32 v24, s15, 8, v2
	v_and_or_b32 v24, v24, s20, v31
	v_lshlrev_b32_e32 v25, 10, v24
	v_or_b32_e32 v122, v25, v32
	v_bfe_i32 v25, v24, 0, 22
	v_bfe_u32 v24, v24, 21, 1
	v_add_u32_e32 v28, v25, v24
	v_lshlrev_b32_e32 v24, 3, v28
	v_and_b32_e32 v28, 0x7fffffe, v28
	v_sub_u32_e32 v25, v25, v28
	v_lshl_or_b32 v28, v25, 5, v34
	v_lshlrev_b32_e32 v25, 10, v35
	v_or_b32_e32 v126, v25, v32
	v_lshlrev_b32_e32 v25, 10, v36
	v_or_b32_e32 v127, v25, v32
	v_xad_u32 v25, s17, 16, v2
	v_and_or_b32 v25, v25, s20, v31
	v_lshlrev_b32_e32 v29, 10, v25
	v_or_b32_e32 v123, v29, v32
	v_bfe_i32 v29, v25, 0, 22
	v_bfe_u32 v25, v25, 21, 1
	v_add_u32_e32 v25, v29, v25
	v_and_b32_e32 v121, 3, v2
	v_lshlrev_b32_e32 v30, 3, v25
	v_and_b32_e32 v25, 0x7fffffe, v25
	v_xad_u32 v2, s17, 24, v2
	v_sub_u32_e32 v25, v29, v25
	v_and_or_b32 v2, v2, s20, v31
	v_lshl_or_b32 v106, v25, 5, v34
	v_lshlrev_b32_e32 v25, 10, v2
	v_or_b32_e32 v124, v25, v32
	v_bfe_i32 v25, v2, 0, 22
	v_bfe_u32 v2, v2, 21, 1
	v_add_u32_e32 v2, v25, v2
	v_lshlrev_b32_e32 v29, 3, v2
	v_and_b32_e32 v2, 0x7fffffe, v2
	v_and_b32_e32 v118, 15, v0
	v_sub_u32_e32 v2, v25, v2
	v_lshlrev_b32_e32 v25, 2, v0
	v_ashrrev_i32_e32 v120, 8, v0
	v_and_or_b32 v32, v29, -16, v33
	v_lshl_or_b32 v108, v2, 5, v34
	v_and_b32_e32 v2, 48, v0
	v_and_b32_e32 v25, 32, v25
	v_lshlrev_b32_e32 v29, 6, v118
	v_and_b32_e32 v119, 63, v0
	v_and_or_b32 v24, v24, -16, v33
	v_and_or_b32 v30, v30, -16, v33
	v_lshlrev_b32_e32 v68, 13, v120
	v_bitop3_b32 v2, v29, v25, v2 bitop3:0x36
	v_ashrrev_i32_e32 v25, 31, v24
	v_lshlrev_b64 v[24:25], 12, v[24:25]
	v_lshl_add_u64 v[56:57], s[6:7], 0, v[24:25]
	v_ashrrev_i32_e32 v29, 31, v28
	v_lshl_add_u64 v[24:25], v[56:57], 0, s[0:1]
	v_lshlrev_b64 v[58:59], 2, v[28:29]
	v_ashrrev_i32_e32 v31, 31, v30
	v_lshl_add_u64 v[24:25], v[24:25], 0, v[58:59]
	v_lshlrev_b64 v[110:111], 11, v[30:31]
	v_ashrrev_i32_e32 v107, 31, v106
	v_ashrrev_i32_e32 v33, 31, v32
	global_load_dwordx4 v[40:43], v[24:25], off offset:16
	global_load_dwordx4 v[44:47], v[24:25], off
	v_lshl_add_u64 v[24:25], s[2:3], 0, v[110:111]
	v_lshlrev_b64 v[60:61], 1, v[106:107]
	v_lshlrev_b64 v[112:113], 11, v[32:33]
	v_ashrrev_i32_e32 v109, 31, v108
	v_lshl_add_u64 v[24:25], v[24:25], 0, v[60:61]
	v_lshl_add_u64 v[28:29], s[2:3], 0, v[112:113]
	v_lshlrev_b64 v[62:63], 1, v[108:109]
	v_lshl_add_u64 v[28:29], v[28:29], 0, v[62:63]
	global_load_dwordx4 v[48:51], v[24:25], off
	global_load_dwordx4 v[52:55], v[28:29], off
	s_add_i32 s0, s14, 64
	s_and_b32 s2, s0, 0x3c0
	s_lshl_b32 s0, s2, 2
	s_lshl_b32 s2, s2, 1
	v_lshl_add_u64 v[24:25], v[4:5], 0, s[0:1]
	s_add_u32 s2, s12, s2
	v_lshl_add_u64 v[24:25], v[24:25], 0, v[38:39]
	s_addc_u32 s3, s13, 0
	global_load_dwordx4 v[30:33], v[24:25], off offset:16
	global_load_dwordx4 v[34:37], v[24:25], off
	v_lshl_add_u64 v[24:25], s[2:3], 0, v[102:103]
	v_lshl_add_u64 v[64:65], v[24:25], 0, v[22:23]
	v_lshl_add_u64 v[22:23], s[2:3], 0, v[104:105]
	v_lshl_add_u64 v[66:67], v[22:23], 0, v[26:27]
	global_load_dwordx4 v[26:29], v[64:65], off
	global_load_dwordx4 v[22:25], v[66:67], off
	v_add_u32_e32 v64, 0, v125
	s_waitcnt vmcnt(10)
	v_cvt_pk_bf16_f32 v10, v10, v11
	v_cvt_pk_bf16_f32 v11, v12, v13
	v_cvt_pk_bf16_f32 v12, v6, v7
	v_add_u32_e32 v6, 0, v126
	v_cvt_pk_bf16_f32 v13, v8, v9
	ds_write_b128 v64, v[10:13]
	s_waitcnt vmcnt(9)
	ds_write_b128 v6, v[14:17] offset:32768
	v_add_u32_e32 v6, 0, v127
	s_waitcnt vmcnt(8)
	ds_write_b128 v6, v[18:21] offset:32768
	v_add_u32_e32 v10, 0, v122
	s_waitcnt vmcnt(6)
	v_cvt_pk_bf16_f32 v6, v44, v45
	v_cvt_pk_bf16_f32 v7, v46, v47
	v_cvt_pk_bf16_f32 v8, v40, v41
	v_cvt_pk_bf16_f32 v9, v42, v43
	ds_write_b128 v10, v[6:9]
	v_add_u32_e32 v6, 0, v123
	s_waitcnt vmcnt(5)
	ds_write_b128 v6, v[48:51] offset:32768
	v_add_u32_e32 v6, 0, v124
	s_waitcnt vmcnt(4)
	ds_write_b128 v6, v[52:55] offset:32768
	v_lshl_add_u64 v[6:7], v[56:57], 0, s[0:1]
	v_lshl_add_u64 v[14:15], v[6:7], 0, v[58:59]
	global_load_dwordx4 v[6:9], v[14:15], off offset:16
	global_load_dwordx4 v[10:13], v[14:15], off
	v_lshl_add_u64 v[14:15], s[2:3], 0, v[110:111]
	v_lshl_add_u64 v[40:41], v[14:15], 0, v[60:61]
	v_lshl_add_u64 v[14:15], s[2:3], 0, v[112:113]
	v_lshl_add_u64 v[42:43], v[14:15], 0, v[62:63]
	global_load_dwordx4 v[18:21], v[40:41], off
	global_load_dwordx4 v[14:17], v[42:43], off
	v_lshlrev_b32_e32 v40, 13, v121
	s_cmp_lg_u32 0, -1
	s_waitcnt lgkmcnt(0)
	s_cselect_b32 s0, 0, 0
	v_add3_u32 v128, v68, s0, v2
	s_add_i32 s0, s0, 0x8000
	v_add3_u32 v129, v40, s0, v2
	v_lshl_add_u64 v[114:115], v[4:5], 0, v[38:39]
	v_lshl_add_u64 v[116:117], v[56:57], 0, v[58:59]
	s_add_i32 s2, s14, 0x80
	s_mov_b32 s3, 0
	v_mov_b32_e32 v2, v3
	v_mov_b32_e32 v4, v3
	v_mov_b32_e32 v5, v3
	v_mov_b32_e32 v38, v3
	v_mov_b32_e32 v39, v3
	v_mov_b32_e32 v40, v3
	v_mov_b32_e32 v41, v3
	v_mov_b32_e32 v42, v3
	v_mov_b32_e32 v43, v3
	v_mov_b32_e32 v44, v3
	v_mov_b32_e32 v45, v3
	v_mov_b32_e32 v46, v3
	v_mov_b32_e32 v47, v3
	v_mov_b32_e32 v48, v3
	v_mov_b32_e32 v49, v3
	v_mov_b32_e32 v50, v3
	v_mov_b32_e32 v51, v3
	v_mov_b32_e32 v52, v3
	v_mov_b32_e32 v53, v3
	v_mov_b32_e32 v54, v3
	v_mov_b32_e32 v55, v3
	v_mov_b32_e32 v56, v3
	v_mov_b32_e32 v57, v3
	v_mov_b32_e32 v58, v3
	v_mov_b32_e32 v59, v3
	v_mov_b32_e32 v60, v3
	v_mov_b32_e32 v61, v3
	v_mov_b32_e32 v62, v3
	v_mov_b32_e32 v63, v3
	v_mov_b32_e32 v64, v3
	v_mov_b32_e32 v65, v3
	v_mov_b32_e32 v66, v3
	v_mov_b32_e32 v67, v3
	v_mov_b32_e32 v68, v3
	v_mov_b32_e32 v69, v3
	v_mov_b32_e32 v70, v3
	v_mov_b32_e32 v71, v3
	v_mov_b32_e32 v72, v3
	v_mov_b32_e32 v73, v3
	v_mov_b32_e32 v74, v3
	v_mov_b32_e32 v75, v3
	v_mov_b32_e32 v76, v3
	v_mov_b32_e32 v77, v3
	v_mov_b32_e32 v78, v3
	v_mov_b32_e32 v79, v3
	v_mov_b32_e32 v80, v3
	v_mov_b32_e32 v81, v3
	v_mov_b32_e32 v82, v3
	v_mov_b32_e32 v83, v3
	v_mov_b32_e32 v84, v3
	v_mov_b32_e32 v85, v3
	v_mov_b32_e32 v86, v3
	v_mov_b32_e32 v87, v3
	v_mov_b32_e32 v88, v3
	v_mov_b32_e32 v89, v3
	v_mov_b32_e32 v90, v3
	v_mov_b32_e32 v91, v3
	v_mov_b32_e32 v92, v3
	v_mov_b32_e32 v93, v3
	v_mov_b32_e32 v94, v3
	v_mov_b32_e32 v95, v3
	v_mov_b32_e32 v96, v3
	v_mov_b32_e32 v97, v3
	s_barrier
.LBB1_3:
	s_and_b32 s0, s3, 0x10000
	v_add_u32_e32 v158, s0, v128
	v_add_u32_e32 v159, s0, v129
	ds_read_b128 v[130:133], v159 offset:0
	ds_read_b128 v[134:137], v159 offset:2048
	ds_read_b128 v[138:141], v159 offset:4096
	ds_read_b128 v[142:145], v159 offset:6144
	ds_read_b128 v[146:149], v158 offset:0
	ds_read_b128 v[150:153], v158 offset:2048
	ds_read_b128 v[154:157], v158 offset:4096
	ds_read_b128 v[160:163], v158 offset:6144
	s_waitcnt lgkmcnt(3)
	v_mfma_f32_16x16x32_bf16 v[94:97], v[130:133], v[146:149], v[94:97]
	v_mfma_f32_16x16x32_bf16 v[90:93], v[134:137], v[146:149], v[90:93]
	v_mfma_f32_16x16x32_bf16 v[86:89], v[138:141], v[146:149], v[86:89]
	v_mfma_f32_16x16x32_bf16 v[82:85], v[142:145], v[146:149], v[82:85]
	s_waitcnt lgkmcnt(2)
	v_mfma_f32_16x16x32_bf16 v[78:81], v[130:133], v[150:153], v[78:81]
	v_mfma_f32_16x16x32_bf16 v[74:77], v[134:137], v[150:153], v[74:77]
	v_mfma_f32_16x16x32_bf16 v[70:73], v[138:141], v[150:153], v[70:73]
	v_mfma_f32_16x16x32_bf16 v[66:69], v[142:145], v[150:153], v[66:69]
	s_waitcnt lgkmcnt(1)
	v_mfma_f32_16x16x32_bf16 v[62:65], v[130:133], v[154:157], v[62:65]
	v_mfma_f32_16x16x32_bf16 v[58:61], v[134:137], v[154:157], v[58:61]
	v_mfma_f32_16x16x32_bf16 v[54:57], v[138:141], v[154:157], v[54:57]
	v_mfma_f32_16x16x32_bf16 v[50:53], v[142:145], v[154:157], v[50:53]
	s_waitcnt lgkmcnt(0)
	v_mfma_f32_16x16x32_bf16 v[46:49], v[130:133], v[160:163], v[46:49]
	v_mfma_f32_16x16x32_bf16 v[42:45], v[134:137], v[160:163], v[42:45]
	v_mfma_f32_16x16x32_bf16 v[38:41], v[138:141], v[160:163], v[38:41]
	v_mfma_f32_16x16x32_bf16 v[2:5], v[142:145], v[160:163], v[2:5]
	s_xor_b32 s0, s0, 0x10000
	s_and_b32 s6, s2, 0x3c0
	s_add_i32 s14, s0, 0
	s_lshl_b32 s0, s6, 2
	s_lshl_b32 s6, s6, 1
	s_add_u32 s6, s12, s6
	s_waitcnt vmcnt(6)
	v_cvt_pk_bf16_f32 v34, v34, v35
	v_cvt_pk_bf16_f32 v35, v36, v37
	v_cvt_pk_bf16_f32 v36, v30, v31
	v_cvt_pk_bf16_f32 v37, v32, v33
	v_add_u32_e32 v30, s14, v125
	s_addc_u32 s7, s13, 0
	v_add_u32_e32 v31, s14, v126
	v_add_u32_e32 v32, s14, v127
	ds_write_b128 v30, v[34:37]
	s_waitcnt vmcnt(5)
	ds_write_b128 v31, v[26:29] offset:32768
	s_waitcnt vmcnt(4)
	ds_write_b128 v32, v[22:25] offset:32768
	v_lshl_add_u64 v[22:23], s[6:7], 0, v[102:103]
	v_lshl_add_u64 v[24:25], s[6:7], 0, v[104:105]
	v_lshl_add_u64 v[130:131], v[114:115], 0, s[0:1]
	v_lshl_add_u64 v[22:23], v[98:99], 1, v[22:23]
	v_lshl_add_u64 v[24:25], v[100:101], 1, v[24:25]
	global_load_dwordx4 v[30:33], v[130:131], off offset:16
	global_load_dwordx4 v[34:37], v[130:131], off
	global_load_dwordx4 v[26:29], v[22:23], off
	s_nop 0
	global_load_dwordx4 v[22:25], v[24:25], off
	ds_read_b128 v[130:133], v159 offset:1024
	ds_read_b128 v[134:137], v159 offset:3072
	ds_read_b128 v[138:141], v159 offset:5120
	ds_read_b128 v[142:145], v159 offset:7168
	ds_read_b128 v[146:149], v158 offset:1024
	ds_read_b128 v[150:153], v158 offset:3072
	ds_read_b128 v[154:157], v158 offset:5120
	ds_read_b128 v[160:163], v158 offset:7168
	s_waitcnt lgkmcnt(3)
	v_mfma_f32_16x16x32_bf16 v[94:97], v[130:133], v[146:149], v[94:97]
	v_mfma_f32_16x16x32_bf16 v[90:93], v[134:137], v[146:149], v[90:93]
	v_mfma_f32_16x16x32_bf16 v[86:89], v[138:141], v[146:149], v[86:89]
	v_mfma_f32_16x16x32_bf16 v[82:85], v[142:145], v[146:149], v[82:85]
	s_waitcnt lgkmcnt(2)
	v_mfma_f32_16x16x32_bf16 v[78:81], v[130:133], v[150:153], v[78:81]
	v_mfma_f32_16x16x32_bf16 v[74:77], v[134:137], v[150:153], v[74:77]
	v_mfma_f32_16x16x32_bf16 v[70:73], v[138:141], v[150:153], v[70:73]
	v_mfma_f32_16x16x32_bf16 v[66:69], v[142:145], v[150:153], v[66:69]
	s_waitcnt lgkmcnt(1)
	v_mfma_f32_16x16x32_bf16 v[62:65], v[130:133], v[154:157], v[62:65]
	v_mfma_f32_16x16x32_bf16 v[58:61], v[134:137], v[154:157], v[58:61]
	v_mfma_f32_16x16x32_bf16 v[54:57], v[138:141], v[154:157], v[54:57]
	v_mfma_f32_16x16x32_bf16 v[50:53], v[142:145], v[154:157], v[50:53]
	s_waitcnt lgkmcnt(0)
	v_mfma_f32_16x16x32_bf16 v[46:49], v[130:133], v[160:163], v[46:49]
	v_mfma_f32_16x16x32_bf16 v[42:45], v[134:137], v[160:163], v[42:45]
	v_mfma_f32_16x16x32_bf16 v[38:41], v[138:141], v[160:163], v[38:41]
	v_mfma_f32_16x16x32_bf16 v[2:5], v[142:145], v[160:163], v[2:5]
	v_add_u32_e32 v130, s14, v122
	s_waitcnt vmcnt(6)
	v_cvt_pk_bf16_f32 v10, v10, v11
	v_cvt_pk_bf16_f32 v11, v12, v13
	v_cvt_pk_bf16_f32 v12, v6, v7
	v_add_u32_e32 v6, s14, v123
	v_cvt_pk_bf16_f32 v13, v8, v9
	ds_write_b128 v130, v[10:13]
	s_waitcnt vmcnt(5)
	ds_write_b128 v6, v[18:21] offset:32768
	v_add_u32_e32 v6, s14, v124
	s_waitcnt vmcnt(4)
	ds_write_b128 v6, v[14:17] offset:32768
	v_lshl_add_u64 v[14:15], s[6:7], 0, v[110:111]
	v_lshl_add_u64 v[16:17], s[6:7], 0, v[112:113]
	v_lshl_add_u64 v[10:11], v[116:117], 0, s[0:1]
	v_lshl_add_u64 v[14:15], v[106:107], 1, v[14:15]
	v_lshl_add_u64 v[16:17], v[108:109], 1, v[16:17]
	global_load_dwordx4 v[6:9], v[10:11], off offset:16
	s_nop 0
	global_load_dwordx4 v[10:13], v[10:11], off
	s_nop 0
	global_load_dwordx4 v[18:21], v[14:15], off
	s_nop 0
	global_load_dwordx4 v[14:17], v[16:17], off
	s_waitcnt lgkmcnt(0)
	s_add_i32 s2, s2, 64
	s_add_i32 s3, s3, 0x10000
	s_cmp_lg_u32 s3, 0xe0000
	s_barrier
	s_cbranch_scc1 .LBB1_3
	ds_read_b128 v[98:101], v129 offset:0
	ds_read_b128 v[102:105], v129 offset:0x800
	ds_read_b128 v[106:109], v129 offset:0x1000
	ds_read_b128 v[110:113], v129 offset:0x1800
	ds_read_b128 v[114:117], v128 offset:0
	ds_read_b128 v[130:133], v128 offset:0x800
	ds_read_b128 v[134:137], v128 offset:0x1000
	s_waitcnt lgkmcnt(2)
	v_mfma_f32_16x16x32_bf16 v[94:97], v[98:101], v[114:117], v[94:97]
	v_mfma_f32_16x16x32_bf16 v[90:93], v[102:105], v[114:117], v[90:93]
	v_mfma_f32_16x16x32_bf16 v[86:89], v[106:109], v[114:117], v[86:89]
	v_mfma_f32_16x16x32_bf16 v[82:85], v[110:113], v[114:117], v[82:85]
	ds_read_b128 v[114:117], v128 offset:0x1800
	s_waitcnt lgkmcnt(2)
	v_mfma_f32_16x16x32_bf16 v[78:81], v[98:101], v[130:133], v[78:81]
	v_mfma_f32_16x16x32_bf16 v[74:77], v[102:105], v[130:133], v[74:77]
	v_mfma_f32_16x16x32_bf16 v[70:73], v[106:109], v[130:133], v[70:73]
	v_mfma_f32_16x16x32_bf16 v[66:69], v[110:113], v[130:133], v[66:69]
	s_waitcnt lgkmcnt(1)
	v_mfma_f32_16x16x32_bf16 v[62:65], v[98:101], v[134:137], v[62:65]
	v_mfma_f32_16x16x32_bf16 v[58:61], v[102:105], v[134:137], v[58:61]
	v_mfma_f32_16x16x32_bf16 v[54:57], v[106:109], v[134:137], v[54:57]
	v_mfma_f32_16x16x32_bf16 v[50:53], v[110:113], v[134:137], v[50:53]
	s_waitcnt lgkmcnt(0)
	v_mfma_f32_16x16x32_bf16 v[46:49], v[98:101], v[114:117], v[46:49]
	v_mfma_f32_16x16x32_bf16 v[42:45], v[102:105], v[114:117], v[42:45]
	v_mfma_f32_16x16x32_bf16 v[38:41], v[106:109], v[114:117], v[38:41]
	v_mfma_f32_16x16x32_bf16 v[2:5], v[110:113], v[114:117], v[2:5]
	v_add_u32_e32 v98, s18, v125
	s_waitcnt vmcnt(6)
	v_cvt_pk_bf16_f32 v34, v34, v35
	v_cvt_pk_bf16_f32 v35, v36, v37
	v_cvt_pk_bf16_f32 v36, v30, v31
	v_add_u32_e32 v30, s19, v126
	v_cvt_pk_bf16_f32 v37, v32, v33
	ds_write_b128 v98, v[34:37]
	s_waitcnt vmcnt(5)
	ds_write_b128 v30, v[26:29]
	v_add_u32_e32 v26, s19, v127
	s_waitcnt vmcnt(4)
	ds_write_b128 v26, v[22:25]
	ds_read_b128 v[22:25], v129 offset:0x400
	ds_read_b128 v[26:29], v129 offset:0xc00
	ds_read_b128 v[30:33], v129 offset:0x1400
	ds_read_b128 v[34:37], v129 offset:0x1c00
	ds_read_b128 v[98:101], v128 offset:0x400
	ds_read_b128 v[102:105], v128 offset:0xc00
	ds_read_b128 v[106:109], v128 offset:0x1400
	s_waitcnt lgkmcnt(2)
	v_mfma_f32_16x16x32_bf16 v[94:97], v[22:25], v[98:101], v[94:97]
	v_mfma_f32_16x16x32_bf16 v[90:93], v[26:29], v[98:101], v[90:93]
	v_mfma_f32_16x16x32_bf16 v[86:89], v[30:33], v[98:101], v[86:89]
	v_mfma_f32_16x16x32_bf16 v[82:85], v[34:37], v[98:101], v[82:85]
	ds_read_b128 v[98:101], v128 offset:0x1c00
	s_waitcnt lgkmcnt(2)
	v_mfma_f32_16x16x32_bf16 v[78:81], v[22:25], v[102:105], v[78:81]
	v_mfma_f32_16x16x32_bf16 v[74:77], v[26:29], v[102:105], v[74:77]
	v_mfma_f32_16x16x32_bf16 v[70:73], v[30:33], v[102:105], v[70:73]
	v_mfma_f32_16x16x32_bf16 v[66:69], v[34:37], v[102:105], v[66:69]
	s_waitcnt lgkmcnt(1)
	v_mfma_f32_16x16x32_bf16 v[62:65], v[22:25], v[106:109], v[62:65]
	v_mfma_f32_16x16x32_bf16 v[58:61], v[26:29], v[106:109], v[58:61]
	v_mfma_f32_16x16x32_bf16 v[54:57], v[30:33], v[106:109], v[54:57]
	v_mfma_f32_16x16x32_bf16 v[50:53], v[34:37], v[106:109], v[50:53]
	s_waitcnt lgkmcnt(0)
	v_mfma_f32_16x16x32_bf16 v[22:25], v[22:25], v[98:101], v[46:49]
	v_mfma_f32_16x16x32_bf16 v[26:29], v[26:29], v[98:101], v[42:45]
	v_mfma_f32_16x16x32_bf16 v[30:33], v[30:33], v[98:101], v[38:41]
	v_mfma_f32_16x16x32_bf16 v[2:5], v[34:37], v[98:101], v[2:5]
	v_add_u32_e32 v34, s18, v122
	s_waitcnt vmcnt(2)
	v_cvt_pk_bf16_f32 v10, v10, v11
	v_cvt_pk_bf16_f32 v11, v12, v13
	v_cvt_pk_bf16_f32 v12, v6, v7
	v_add_u32_e32 v6, s19, v123
	s_lshl_b64 s[0:1], s[4:5], 1
	v_cvt_pk_bf16_f32 v13, v8, v9
	ds_write_b128 v34, v[10:13]
	s_waitcnt vmcnt(1)
	ds_write_b128 v6, v[18:21]
	v_add_u32_e32 v6, s19, v124
	s_add_u32 s0, s10, s0
	s_waitcnt vmcnt(0)
	ds_write_b128 v6, v[14:17]
	s_addc_u32 s1, s11, s1
	s_lshl_b32 s2, s16, 9
	s_waitcnt lgkmcnt(0)
	s_barrier
	v_add_u32_e32 v110, 0x10000, v128
	v_add_u32_e32 v102, 0x10000, v129
	ds_read_b128 v[6:9], v102 offset:0
	ds_read_b128 v[10:13], v102 offset:0x800
	ds_read_b128 v[14:17], v102 offset:0x1000
	ds_read_b128 v[18:21], v102 offset:0x1800
	ds_read_b128 v[34:37], v110 offset:0
	ds_read_b128 v[38:41], v110 offset:0x800
	ds_read_b128 v[42:45], v110 offset:0x1000
	s_add_u32 s0, s0, s2
	s_addc_u32 s1, s1, 0
	s_lshl_b32 s2, s16, 10
	s_waitcnt lgkmcnt(2)
	s_add_u32 s2, s8, s2
	v_mfma_f32_16x16x32_bf16 v[46:49], v[6:9], v[34:37], v[94:97]
	s_addc_u32 s3, s9, 0
	v_mfma_f32_16x16x32_bf16 v[90:93], v[10:13], v[34:37], v[90:93]
	v_mfma_f32_16x16x32_bf16 v[86:89], v[14:17], v[34:37], v[86:89]
	v_mfma_f32_16x16x32_bf16 v[34:37], v[18:21], v[34:37], v[82:85]
	ds_read_b128 v[82:85], v110 offset:0x1800
	s_waitcnt lgkmcnt(2)
	v_mfma_f32_16x16x32_bf16 v[78:81], v[6:9], v[38:41], v[78:81]
	v_mfma_f32_16x16x32_bf16 v[74:77], v[10:13], v[38:41], v[74:77]
	v_mfma_f32_16x16x32_bf16 v[70:73], v[14:17], v[38:41], v[70:73]
	v_mfma_f32_16x16x32_bf16 v[38:41], v[18:21], v[38:41], v[66:69]
	s_waitcnt lgkmcnt(1)
	v_mfma_f32_16x16x32_bf16 v[62:65], v[6:9], v[42:45], v[62:65]
	v_mfma_f32_16x16x32_bf16 v[58:61], v[10:13], v[42:45], v[58:61]
	v_mfma_f32_16x16x32_bf16 v[54:57], v[14:17], v[42:45], v[54:57]
	v_mfma_f32_16x16x32_bf16 v[42:45], v[18:21], v[42:45], v[50:53]
	s_waitcnt lgkmcnt(0)
	v_mfma_f32_16x16x32_bf16 v[50:53], v[6:9], v[82:85], v[22:25]
	v_mfma_f32_16x16x32_bf16 v[66:69], v[10:13], v[82:85], v[26:29]
	v_mfma_f32_16x16x32_bf16 v[94:97], v[14:17], v[82:85], v[30:33]
	v_mfma_f32_16x16x32_bf16 v[2:5], v[18:21], v[82:85], v[2:5]
	ds_read_b128 v[18:21], v102 offset:0x400
	ds_read_b128 v[82:85], v102 offset:0xc00
	ds_read_b128 v[98:101], v102 offset:0x1400
	ds_read_b128 v[102:105], v102 offset:0x1c00
	ds_read_b128 v[6:9], v110 offset:0x400
	ds_read_b128 v[10:13], v110 offset:0xc00
	ds_read_b128 v[106:109], v110 offset:0x1400
	s_waitcnt lgkmcnt(2)
	v_mfma_f32_16x16x32_bf16 v[46:49], v[18:21], v[6:9], v[46:49]
	v_mfma_f32_16x16x32_bf16 v[90:93], v[82:85], v[6:9], v[90:93]
	v_mfma_f32_16x16x32_bf16 v[30:33], v[98:101], v[6:9], v[86:89]
	v_mfma_f32_16x16x32_bf16 v[14:17], v[102:105], v[6:9], v[34:37]
	ds_read_b128 v[86:89], v110 offset:0x1c00
	s_waitcnt lgkmcnt(2)
	v_mfma_f32_16x16x32_bf16 v[78:81], v[18:21], v[10:13], v[78:81]
	v_mfma_f32_16x16x32_bf16 v[74:77], v[82:85], v[10:13], v[74:77]
	v_mfma_f32_16x16x32_bf16 v[26:29], v[98:101], v[10:13], v[70:73]
	v_mfma_f32_16x16x32_bf16 v[10:13], v[102:105], v[10:13], v[38:41]
	s_waitcnt lgkmcnt(1)
	v_mfma_f32_16x16x32_bf16 v[62:65], v[18:21], v[106:109], v[62:65]
	v_mfma_f32_16x16x32_bf16 v[38:41], v[82:85], v[106:109], v[58:61]
	v_mfma_f32_16x16x32_bf16 v[22:25], v[98:101], v[106:109], v[54:57]
	v_mfma_f32_16x16x32_bf16 v[6:9], v[102:105], v[106:109], v[42:45]
	s_waitcnt lgkmcnt(0)
	v_mfma_f32_16x16x32_bf16 v[42:45], v[18:21], v[86:89], v[50:53]
	v_mfma_f32_16x16x32_bf16 v[34:37], v[82:85], v[86:89], v[66:69]
	v_mfma_f32_16x16x32_bf16 v[18:21], v[98:101], v[86:89], v[94:97]
	v_mfma_f32_16x16x32_bf16 v[2:5], v[102:105], v[86:89], v[2:5]
	v_lshrrev_b32_e32 v50, 2, v119
	v_and_b32_e32 v50, 12, v50
	v_lshl_or_b32 v66, v121, 6, v50
	v_lshlrev_b32_e32 v67, 2, v66
	s_waitcnt lgkmcnt(0)
	s_barrier
	global_load_dwordx4 v[50:53], v67, s[2:3]
	global_load_dwordx4 v[54:57], v67, s[2:3] offset:64
	v_lshrrev_b32_e32 v58, 1, v119
	v_lshl_or_b32 v59, v120, 6, v118
	v_and_b32_e32 v68, 8, v58
	v_lshl_add_u32 v69, v59, 9, 0
	v_or_b32_e32 v70, 16, v59
	v_or_b32_e32 v71, 48, v59
	v_lshrrev_b32_e32 v58, 3, v66
	v_or_b32_e32 v59, 16, v66
	v_bitop3_b32 v83, v70, v58, 31 bitop3:0x6c
	v_lshrrev_b32_e32 v85, 3, v59
	v_lshl_add_u32 v72, v70, 9, 0
	v_xor_b32_e32 v82, v58, v118
	v_bitop3_b32 v84, v71, v58, 31 bitop3:0x6c
	v_lshlrev_b32_e32 v83, 4, v83
	v_xor_b32_e32 v86, v85, v118
	v_lshl_add_u32 v73, v71, 9, 0
	v_lshlrev_b32_e32 v82, 4, v82
	v_lshlrev_b32_e32 v84, 4, v84
	v_add3_u32 v83, v72, v83, v68
	v_lshlrev_b32_e32 v86, 4, v86
	global_load_dwordx4 v[58:61], v67, s[2:3] offset:128
	v_add3_u32 v82, v69, v82, v68
	v_add3_u32 v84, v73, v84, v68
	v_add3_u32 v86, v69, v86, v68
	s_waitcnt vmcnt(2)
	v_add_f32_e32 v46, v46, v50
	v_add_f32_e32 v47, v47, v51
	v_add_f32_e32 v48, v48, v52
	v_add_f32_e32 v49, v49, v53
	v_add_f32_e32 v78, v78, v50
	v_add_f32_e32 v79, v79, v51
	v_add_f32_e32 v80, v80, v52
	v_add_f32_e32 v81, v81, v53
	v_add_f32_e32 v62, v62, v50
	v_add_f32_e32 v63, v63, v51
	v_add_f32_e32 v42, v42, v50
	v_add_f32_e32 v43, v43, v51
	v_add_f32_e32 v44, v44, v52
	v_add_f32_e32 v45, v45, v53
	s_waitcnt vmcnt(1)
	v_add_f32_e32 v50, v90, v54
	v_add_f32_e32 v51, v91, v55
	v_add_f32_e32 v64, v64, v52
	v_add_f32_e32 v65, v65, v53
	v_add_f32_e32 v52, v92, v56
	v_add_f32_e32 v53, v93, v57
	v_max_f32_e32 v46, 0, v46
	v_max_f32_e32 v47, 0, v47
	v_max_f32_e32 v48, 0, v48
	v_max_f32_e32 v49, 0, v49
	v_max_f32_e32 v78, 0, v78
	v_max_f32_e32 v79, 0, v79
	v_max_f32_e32 v80, 0, v80
	v_max_f32_e32 v81, 0, v81
	v_max_f32_e32 v88, 0, v43
	v_max_f32_e32 v89, 0, v44
	v_max_f32_e32 v90, 0, v45
	v_max_f32_e32 v50, 0, v50
	v_max_f32_e32 v51, 0, v51
	v_cvt_pk_bf16_f32 v43, v48, v49
	v_cvt_pk_bf16_f32 v44, v78, v79
	v_cvt_pk_bf16_f32 v45, v80, v81
	v_max_f32_e32 v62, 0, v62
	v_max_f32_e32 v63, 0, v63
	v_max_f32_e32 v64, 0, v64
	v_max_f32_e32 v65, 0, v65
	v_max_f32_e32 v87, 0, v42
	v_max_f32_e32 v52, 0, v52
	v_max_f32_e32 v53, 0, v53
	v_cvt_pk_bf16_f32 v42, v46, v47
	v_cvt_pk_bf16_f32 v46, v62, v63
	v_cvt_pk_bf16_f32 v47, v64, v65
	v_cvt_pk_bf16_f32 v48, v87, v88
	v_cvt_pk_bf16_f32 v49, v89, v90
	v_cvt_pk_bf16_f32 v50, v50, v51
	v_cvt_pk_bf16_f32 v51, v52, v53
	ds_write_b64 v83, v[44:45]
	ds_write2st64_b64 v82, v[42:43], v[46:47] offset1:32
	ds_write_b64 v84, v[48:49]
	ds_write_b64 v86, v[50:51]
	v_add_f32_e32 v43, v76, v56
	v_add_f32_e32 v44, v77, v57
	v_max_f32_e32 v43, 0, v43
	v_max_f32_e32 v44, 0, v44
	v_add_f32_e32 v42, v75, v55
	v_cvt_pk_bf16_f32 v43, v43, v44
	v_bitop3_b32 v44, v85, v70, 31 bitop3:0x78
	v_add_f32_e32 v74, v74, v54
	v_max_f32_e32 v42, 0, v42
	v_lshlrev_b32_e32 v44, 4, v44
	v_max_f32_e32 v74, 0, v74
	v_cvt_pk_bf16_f32 v42, v74, v42
	v_add3_u32 v44, v72, v44, v68
	ds_write_b64 v44, v[42:43]
	global_load_dwordx4 v[42:45], v67, s[2:3] offset:192
	v_add_f32_e32 v34, v34, v54
	v_add_f32_e32 v35, v35, v55
	v_add_f32_e32 v36, v36, v56
	v_max_f32_e32 v34, 0, v34
	v_max_f32_e32 v35, 0, v35
	v_max_f32_e32 v36, 0, v36
	v_add_f32_e32 v37, v37, v57
	v_max_f32_e32 v37, 0, v37
	v_cvt_pk_bf16_f32 v34, v34, v35
	v_cvt_pk_bf16_f32 v35, v36, v37
	v_bitop3_b32 v36, v85, v71, 31 bitop3:0x78
	v_add_f32_e32 v38, v38, v54
	v_add_f32_e32 v39, v39, v55
	v_lshlrev_b32_e32 v36, 4, v36
	v_max_f32_e32 v38, 0, v38
	v_max_f32_e32 v39, 0, v39
	v_add_f32_e32 v40, v40, v56
	v_add_f32_e32 v41, v41, v57
	v_add3_u32 v36, v73, v36, v68
	v_max_f32_e32 v40, 0, v40
	v_max_f32_e32 v41, 0, v41
	v_cvt_pk_bf16_f32 v38, v38, v39
	v_cvt_pk_bf16_f32 v39, v40, v41
	ds_write_b64 v86, v[38:39] offset:16384
	ds_write_b64 v36, v[34:35]
	v_or_b32_e32 v34, 32, v66
	s_waitcnt vmcnt(1)
	v_add_f32_e32 v30, v30, v58
	v_add_f32_e32 v31, v31, v59
	v_add_f32_e32 v32, v32, v60
	v_add_f32_e32 v26, v26, v58
	v_add_f32_e32 v27, v27, v59
	v_add_f32_e32 v28, v28, v60
	v_add_f32_e32 v18, v18, v58
	v_add_f32_e32 v19, v19, v59
	v_add_f32_e32 v20, v20, v60
	v_lshrrev_b32_e32 v34, 3, v34
	v_max_f32_e32 v30, 0, v30
	v_max_f32_e32 v31, 0, v31
	v_max_f32_e32 v32, 0, v32
	v_add_f32_e32 v33, v33, v61
	v_max_f32_e32 v26, 0, v26
	v_max_f32_e32 v27, 0, v27
	v_max_f32_e32 v28, 0, v28
	v_add_f32_e32 v29, v29, v61
	v_max_f32_e32 v18, 0, v18
	v_max_f32_e32 v19, 0, v19
	v_max_f32_e32 v20, 0, v20
	v_add_f32_e32 v21, v21, v61
	v_max_f32_e32 v33, 0, v33
	v_cvt_pk_bf16_f32 v30, v30, v31
	v_cvt_pk_bf16_f32 v31, v32, v33
	v_xor_b32_e32 v32, v34, v118
	v_max_f32_e32 v29, 0, v29
	v_cvt_pk_bf16_f32 v26, v26, v27
	v_cvt_pk_bf16_f32 v27, v28, v29
	v_bitop3_b32 v28, v34, v70, 31 bitop3:0x78
	v_max_f32_e32 v21, 0, v21
	v_cvt_pk_bf16_f32 v18, v18, v19
	v_cvt_pk_bf16_f32 v19, v20, v21
	v_bitop3_b32 v20, v34, v71, 31 bitop3:0x78
	v_lshlrev_b32_e32 v32, 4, v32
	v_lshlrev_b32_e32 v28, 4, v28
	v_add_f32_e32 v22, v22, v58
	v_add_f32_e32 v23, v23, v59
	v_lshlrev_b32_e32 v20, 4, v20
	v_add3_u32 v32, v69, v32, v68
	v_add3_u32 v28, v72, v28, v68
	v_max_f32_e32 v22, 0, v22
	v_max_f32_e32 v23, 0, v23
	v_add_f32_e32 v24, v24, v60
	v_add_f32_e32 v25, v25, v61
	v_add3_u32 v20, v73, v20, v68
	ds_write_b64 v32, v[30:31]
	ds_write_b64 v28, v[26:27]
	v_max_f32_e32 v24, 0, v24
	v_max_f32_e32 v25, 0, v25
	v_cvt_pk_bf16_f32 v22, v22, v23
	v_cvt_pk_bf16_f32 v23, v24, v25
	ds_write_b64 v32, v[22:23] offset:16384
	ds_write_b64 v20, v[18:19]
	v_or_b32_e32 v18, 48, v66
	s_waitcnt vmcnt(0)
	v_add_f32_e32 v14, v14, v42
	v_add_f32_e32 v15, v15, v43
	v_add_f32_e32 v16, v16, v44
	v_add_f32_e32 v10, v10, v42
	v_add_f32_e32 v11, v11, v43
	v_add_f32_e32 v12, v12, v44
	v_add_f32_e32 v2, v2, v42
	v_add_f32_e32 v3, v3, v43
	v_add_f32_e32 v4, v4, v44
	v_lshrrev_b32_e32 v18, 3, v18
	v_max_f32_e32 v14, 0, v14
	v_max_f32_e32 v15, 0, v15
	v_max_f32_e32 v16, 0, v16
	v_add_f32_e32 v17, v17, v45
	v_max_f32_e32 v10, 0, v10
	v_max_f32_e32 v11, 0, v11
	v_max_f32_e32 v12, 0, v12
	v_add_f32_e32 v13, v13, v45
	v_max_f32_e32 v2, 0, v2
	v_max_f32_e32 v3, 0, v3
	v_max_f32_e32 v4, 0, v4
	v_add_f32_e32 v5, v5, v45
	v_max_f32_e32 v17, 0, v17
	v_cvt_pk_bf16_f32 v14, v14, v15
	v_cvt_pk_bf16_f32 v15, v16, v17
	v_xor_b32_e32 v16, v18, v118
	v_max_f32_e32 v13, 0, v13
	v_cvt_pk_bf16_f32 v10, v10, v11
	v_cvt_pk_bf16_f32 v11, v12, v13
	v_bitop3_b32 v12, v18, v70, 31 bitop3:0x78
	v_max_f32_e32 v5, 0, v5
	v_cvt_pk_bf16_f32 v2, v2, v3
	v_cvt_pk_bf16_f32 v3, v4, v5
	v_bitop3_b32 v4, v18, v71, 31 bitop3:0x78
	v_lshlrev_b32_e32 v16, 4, v16
	v_lshlrev_b32_e32 v12, 4, v12
	v_add_f32_e32 v6, v6, v42
	v_add_f32_e32 v7, v7, v43
	v_lshlrev_b32_e32 v4, 4, v4
	v_add3_u32 v16, v69, v16, v68
	v_add3_u32 v12, v72, v12, v68
	v_max_f32_e32 v6, 0, v6
	v_max_f32_e32 v7, 0, v7
	v_add_f32_e32 v8, v8, v44
	v_add_f32_e32 v9, v9, v45
	v_add3_u32 v4, v73, v4, v68
	ds_write_b64 v16, v[14:15]
	ds_write_b64 v12, v[10:11]
	v_max_f32_e32 v8, 0, v8
	v_max_f32_e32 v9, 0, v9
	v_cvt_pk_bf16_f32 v6, v6, v7
	v_cvt_pk_bf16_f32 v7, v8, v9
	ds_write_b64 v16, v[6:7] offset:16384
	ds_write_b64 v4, v[2:3]
	v_and_b32_e32 v2, 0x1f0, v1
	v_mov_b32_e32 v3, 0
	v_lshl_add_u64 v[2:3], s[0:1], 0, v[2:3]
	s_mov_b64 s[0:1], 0x2000000
	v_ashrrev_i32_e32 v6, 5, v0
	v_lshl_add_u64 v[10:11], v[2:3], 0, s[0:1]
	v_xor_b32_e32 v2, v6, v0
	v_lshlrev_b32_e32 v2, 4, v2
	v_lshlrev_b32_e32 v1, 9, v6
	v_and_b32_e32 v2, 0x1f0, v2
	v_add3_u32 v1, 0, v1, v2
	s_waitcnt lgkmcnt(0)
	s_barrier
	ds_read_b128 v[2:5], v1
	v_ashrrev_i32_e32 v7, 31, v6
	v_add_u32_e32 v1, 0x200, v0
	v_lshlrev_b64 v[6:7], 11, v[6:7]
	v_ashrrev_i32_e32 v14, 5, v1
	v_lshl_add_u64 v[12:13], v[10:11], 0, v[6:7]
	v_xor_b32_e32 v6, v14, v0
	v_lshlrev_b32_e32 v6, 4, v6
	v_lshlrev_b32_e32 v1, 9, v14
	v_and_b32_e32 v6, 0x1f0, v6
	v_add3_u32 v1, 0, v1, v6
	ds_read_b128 v[6:9], v1
	v_ashrrev_i32_e32 v15, 31, v14
	s_waitcnt lgkmcnt(1)
	global_store_dwordx4 v[12:13], v[2:5], off sc1
	v_add_u32_e32 v1, 0x400, v0
	s_nop 0
	v_lshlrev_b64 v[2:3], 11, v[14:15]
	v_lshl_add_u64 v[2:3], v[10:11], 0, v[2:3]
	s_waitcnt lgkmcnt(0)
	global_store_dwordx4 v[2:3], v[6:9], off sc1
	s_nop 1
	v_ashrrev_i32_e32 v6, 5, v1
	v_xor_b32_e32 v2, v6, v0
	v_lshlrev_b32_e32 v2, 4, v2
	v_lshlrev_b32_e32 v1, 9, v6
	v_and_b32_e32 v2, 0x1f0, v2
	v_add3_u32 v1, 0, v1, v2
	ds_read_b128 v[2:5], v1
	v_ashrrev_i32_e32 v7, 31, v6
	v_add_u32_e32 v1, 0x600, v0
	v_lshlrev_b64 v[6:7], 11, v[6:7]
	v_ashrrev_i32_e32 v14, 5, v1
	v_lshl_add_u64 v[12:13], v[10:11], 0, v[6:7]
	v_xor_b32_e32 v6, v14, v0
	v_lshlrev_b32_e32 v6, 4, v6
	v_lshlrev_b32_e32 v1, 9, v14
	v_and_b32_e32 v6, 0x1f0, v6
	v_add3_u32 v1, 0, v1, v6
	ds_read_b128 v[6:9], v1
	v_ashrrev_i32_e32 v15, 31, v14
	s_waitcnt lgkmcnt(1)
	global_store_dwordx4 v[12:13], v[2:5], off sc1
	v_add_u32_e32 v1, 0x800, v0
	s_nop 0
	v_lshlrev_b64 v[2:3], 11, v[14:15]
	v_lshl_add_u64 v[2:3], v[10:11], 0, v[2:3]
	s_waitcnt lgkmcnt(0)
	global_store_dwordx4 v[2:3], v[6:9], off sc1
	s_nop 1
	v_ashrrev_i32_e32 v6, 5, v1
	v_xor_b32_e32 v2, v6, v0
	v_lshlrev_b32_e32 v2, 4, v2
	v_lshlrev_b32_e32 v1, 9, v6
	v_and_b32_e32 v2, 0x1f0, v2
	v_add3_u32 v1, 0, v1, v2
	ds_read_b128 v[2:5], v1
	v_ashrrev_i32_e32 v7, 31, v6
	v_add_u32_e32 v1, 0xa00, v0
	v_lshlrev_b64 v[6:7], 11, v[6:7]
	v_ashrrev_i32_e32 v14, 5, v1
	v_lshl_add_u64 v[12:13], v[10:11], 0, v[6:7]
	v_xor_b32_e32 v6, v14, v0
	v_lshlrev_b32_e32 v6, 4, v6
	v_lshlrev_b32_e32 v1, 9, v14
	v_and_b32_e32 v6, 0x1f0, v6
	v_add3_u32 v1, 0, v1, v6
	ds_read_b128 v[6:9], v1
	v_ashrrev_i32_e32 v15, 31, v14
	s_waitcnt lgkmcnt(1)
	global_store_dwordx4 v[12:13], v[2:5], off sc1
	v_add_u32_e32 v1, 0xc00, v0
	s_nop 0
	v_lshlrev_b64 v[2:3], 11, v[14:15]
	v_lshl_add_u64 v[2:3], v[10:11], 0, v[2:3]
	s_waitcnt lgkmcnt(0)
	global_store_dwordx4 v[2:3], v[6:9], off sc1
	s_nop 1
	v_ashrrev_i32_e32 v6, 5, v1
	v_xor_b32_e32 v2, v6, v0
	v_lshlrev_b32_e32 v2, 4, v2
	v_lshlrev_b32_e32 v1, 9, v6
	v_and_b32_e32 v2, 0x1f0, v2
	v_add3_u32 v1, 0, v1, v2
	ds_read_b128 v[2:5], v1
	v_add_u32_e32 v1, 0xe00, v0
	v_ashrrev_i32_e32 v14, 5, v1
	v_xor_b32_e32 v0, v14, v0
	v_lshlrev_b32_e32 v0, 4, v0
	v_ashrrev_i32_e32 v7, 31, v6
	v_lshlrev_b32_e32 v1, 9, v14
	v_and_b32_e32 v0, 0x1f0, v0
	v_lshlrev_b64 v[6:7], 11, v[6:7]
	v_add3_u32 v0, 0, v1, v0
	v_lshl_add_u64 v[12:13], v[10:11], 0, v[6:7]
	ds_read_b128 v[6:9], v0
	v_ashrrev_i32_e32 v15, 31, v14
	v_lshlrev_b64 v[0:1], 11, v[14:15]
	v_lshl_add_u64 v[0:1], v[10:11], 0, v[0:1]
	s_waitcnt lgkmcnt(1)
	global_store_dwordx4 v[12:13], v[2:5], off sc1
	s_waitcnt lgkmcnt(0)
	global_store_dwordx4 v[0:1], v[6:9], off sc1
	s_endpgm
